# g3 + phase D LN1: 16 wave_sum butterflies per wave via DPP adds (xor 1,2,4,8) and v_permlane16/32_swap adds (xor 16,32) instead of 96 serial ds_bpermute round trips
# speedup vs baseline: 1.0020x; 1.0020x over previous
.LBB0_1437:
	s_and_saveexec_b64 s[8:9], s[2:3]
	s_mov_b64 s[16:17], 0xc00
	ds_write_b32 v159, v3 offset:33280
	s_or_b64 exec, exec, s[8:9]
	s_lshl_b32 s79, s46, 5
	s_add_i32 s10, s79, s86
	s_ashr_i32 s11, s10, 31
	s_lshl_b64 s[8:9], s[10:11], 12
	s_add_u32 s8, s66, s8
	s_addc_u32 s9, s67, s9
	v_lshlrev_b32_e32 v2, 3, v158
	global_load_dwordx2 v[4:5], v2, s[8:9] offset:512
	global_load_dwordx2 v[112:113], v2, s[8:9] offset:1024
	global_load_dwordx2 v[114:115], v2, s[8:9] offset:1536
	global_load_dwordx2 v[116:117], v2, s[8:9]
	global_load_dwordx2 v[118:119], v2, s[8:9] offset:2048
	global_load_dwordx2 v[120:121], v2, s[8:9] offset:2560
	global_load_dwordx2 v[122:123], v2, s[8:9] offset:3072
	global_load_dwordx2 v[124:125], v2, s[8:9] offset:3584
	global_load_dwordx4 v[102:105], v[162:163], off
	global_load_dwordx4 v[94:97], v[162:163], off offset:1024
	global_load_dwordx4 v[106:109], v[164:165], off
	global_load_dwordx4 v[98:101], v[164:165], off offset:1024
	global_load_dwordx4 v[86:89], v[162:163], off offset:2048
	global_load_dwordx4 v[78:81], v[162:163], off offset:3072
	global_load_dwordx4 v[90:93], v[164:165], off offset:2048
	global_load_dwordx4 v[82:85], v[164:165], off offset:3072
	global_load_dwordx4 v[70:73], v[166:167], off
	global_load_dwordx4 v[74:77], v[168:169], off
	global_load_dwordx4 v[62:65], v[170:171], off
	global_load_dwordx4 v[66:69], v[172:173], off
	global_load_dwordx4 v[54:57], v[174:175], off
	global_load_dwordx4 v[58:61], v[176:177], off
	global_load_dwordx4 v[46:49], v[178:179], off
	global_load_dwordx4 v[50:53], v[180:181], off
	v_lshl_add_u64 v[110:111], s[8:9], 0, v[2:3]
	s_movk_i32 s8, 0x1000
	s_waitcnt vmcnt(0)
	v_lshlrev_b32_e32 v209, 16, v4
	v_and_b32_e32 v191, 0xffff0000, v4
	v_lshlrev_b32_e32 v205, 16, v5
	s_waitcnt vmcnt(20)
	v_lshlrev_b32_e32 v208, 16, v116
	v_and_b32_e32 v190, 0xffff0000, v116
	v_lshlrev_b32_e32 v204, 16, v117
	v_and_b32_e32 v207, 0xffff0000, v5
	v_and_b32_e32 v206, 0xffff0000, v117
	v_lshlrev_b32_e32 v193, 16, v113
	v_lshlrev_b32_e32 v192, 16, v112
	v_and_b32_e32 v195, 0xffff0000, v113
	v_and_b32_e32 v194, 0xffff0000, v112
	v_pk_add_f32 v[4:5], v[208:209], v[190:191]
	v_pk_add_f32 v[112:113], v[204:205], v[206:207]
	v_lshlrev_b32_e32 v186, 16, v114
	v_and_b32_e32 v187, 0xffff0000, v114
	v_lshlrev_b32_e32 v188, 16, v115
	v_and_b32_e32 v189, 0xffff0000, v115
	v_pk_add_f32 v[114:115], v[192:193], v[194:195]
	v_pk_add_f32 v[4:5], v[4:5], v[112:113]
	s_waitcnt vmcnt(19)
	v_and_b32_e32 v155, 0xffff0000, v118
	v_pk_add_f32 v[112:113], v[114:115], v[114:115] op_sel:[0,1] op_sel_hi:[1,0]
	v_add_f32_e32 v4, 0, v4
	v_lshlrev_b32_e32 v211, 16, v118
	v_lshlrev_b32_e32 v185, 16, v119
	v_and_b32_e32 v183, 0xffff0000, v119
	v_add_f32_e32 v184, v186, v187
	v_add_f32_e32 v182, v188, v189
	v_mov_b32_e32 v113, v155
	v_add_f32_e32 v210, v4, v5
	s_waitcnt vmcnt(18)
	v_lshlrev_b32_e32 v153, 16, v121
	v_lshlrev_b32_e32 v152, 16, v120
	v_and_b32_e32 v157, 0xffff0000, v121
	v_and_b32_e32 v156, 0xffff0000, v120
	v_pk_add_f32 v[114:115], v[184:185], v[182:183]
	v_pk_add_f32 v[4:5], v[210:211], v[112:113]
	v_pk_add_f32 v[116:117], v[152:153], v[156:157]
	v_pk_add_f32 v[4:5], v[4:5], v[114:115]
	s_waitcnt vmcnt(17)
	v_lshlrev_b32_e32 v144, 16, v122
	v_and_b32_e32 v145, 0xffff0000, v122
	v_lshlrev_b32_e32 v150, 16, v123
	v_and_b32_e32 v151, 0xffff0000, v123
	s_waitcnt vmcnt(16)
	v_lshlrev_b32_e32 v138, 16, v124
	v_and_b32_e32 v139, 0xffff0000, v124
	v_pk_add_f32 v[116:117], v[116:117], v[116:117] op_sel:[0,1] op_sel_hi:[1,0]
	v_pk_add_f32 v[4:5], v[4:5], v[4:5] op_sel:[0,1] op_sel_hi:[1,0]
	v_lshlrev_b32_e32 v149, 16, v125
	v_and_b32_e32 v147, 0xffff0000, v125
	v_add_f32_e32 v148, v144, v145
	v_add_f32_e32 v146, v150, v151
	v_mov_b32_e32 v117, v139
	v_mov_b32_e32 v5, v138
	v_pk_add_f32 v[118:119], v[148:149], v[146:147]
	v_pk_add_f32 v[4:5], v[4:5], v[116:117]
	s_nop 0
	v_pk_add_f32 v[4:5], v[4:5], v[118:119]
	s_nop 0
	v_add_f32_e32 v112, v4, v5
	v_add_co_u32_e32 v4, vcc, s8, v110
	s_waitcnt lgkmcnt(0)
	s_nop 1
	v_add_f32_dpp v112, v112, v112 quad_perm:[1,0,3,2] row_mask:0xf bank_mask:0xf
	v_addc_co_u32_e32 v5, vcc, 0, v111, vcc
	v_add_co_u32_e32 v114, vcc, s89, v110
	s_waitcnt lgkmcnt(0)
	s_nop 1
	v_add_f32_dpp v112, v112, v112 quad_perm:[2,3,0,1] row_mask:0xf bank_mask:0xf
	v_addc_co_u32_e32 v115, vcc, 0, v111, vcc
	global_load_dwordx2 v[132:133], v[4:5], off offset:512
	global_load_dwordx2 v[128:129], v[4:5], off offset:1024
	global_load_dwordx2 v[124:125], v[4:5], off offset:1536
	global_load_dwordx2 v[120:121], v[4:5], off offset:2048
	s_waitcnt lgkmcnt(0)
	s_nop 1
	v_add_f32_dpp v118, v112, v112 row_half_mirror row_mask:0xf bank_mask:0xf
	global_load_dwordx2 v[136:137], v[114:115], off offset:-4096
	global_load_dwordx2 v[116:117], v[4:5], off offset:2560
	global_load_dwordx2 v[112:113], v[4:5], off offset:3072
	s_nop 0
	global_load_dwordx2 v[4:5], v[4:5], off offset:3584
	s_nop 0
	global_load_dwordx2 v[140:141], v[114:115], off
	global_load_dwordx2 v[142:143], v[114:115], off offset:512
	global_load_dwordx2 v[134:135], v[114:115], off offset:1024
	global_load_dwordx2 v[130:131], v[114:115], off offset:1536
	s_waitcnt lgkmcnt(0)
	s_nop 1
	v_add_f32_dpp v118, v118, v118 row_mirror row_mask:0xf bank_mask:0xf
	s_waitcnt lgkmcnt(0)
	v_mov_b32_e32 v119, v118
	v_mov_b32_e32 v146, v118
	s_nop 1
	v_permlane16_swap_b32_e32 v119, v146
	v_add_f32_e32 v146, v146, v119
	global_load_dwordx2 v[126:127], v[114:115], off offset:2048
	global_load_dwordx2 v[122:123], v[114:115], off offset:2560
	global_load_dwordx2 v[118:119], v[114:115], off offset:3072
	s_nop 0
	global_load_dwordx2 v[114:115], v[114:115], off offset:3584
	s_waitcnt lgkmcnt(0)
	v_mov_b32_e32 v148, v146
	s_nop 1
	v_permlane32_swap_b32_e32 v148, v146
	v_add_f32_e32 v146, v146, v148
	v_fmac_f32_e32 v206, 0xba000000, v146
	v_fmac_f32_e32 v190, 0xba000000, v146
	v_fmac_f32_e32 v204, 0xba000000, v146
	v_fmac_f32_e32 v208, 0xba000000, v146
	v_mul_f32_e32 v148, v190, v190
	v_mul_f32_e32 v154, v206, v206
	v_fmac_f32_e32 v207, 0xba000000, v146
	v_fmac_f32_e32 v191, 0xba000000, v146
	v_fmac_f32_e32 v148, v208, v208
	v_fmac_f32_e32 v154, v204, v204
	v_fmac_f32_e32 v205, 0xba000000, v146
	v_fmac_f32_e32 v209, 0xba000000, v146
	v_mul_f32_e32 v182, v191, v191
	v_add_f32_e32 v148, v148, v154
	v_mul_f32_e32 v154, v207, v207
	v_fmac_f32_e32 v182, v209, v209
	v_fmac_f32_e32 v154, v205, v205
	v_add_f32_e32 v154, v182, v154
	v_fmac_f32_e32 v195, 0xba000000, v146
	v_fmac_f32_e32 v194, 0xba000000, v146
	v_add_f32_e32 v148, v148, v154
	v_fmac_f32_e32 v193, 0xba000000, v146
	v_fmac_f32_e32 v192, 0xba000000, v146
	v_mul_f32_e32 v154, v194, v194
	v_mul_f32_e32 v182, v195, v195
	v_fmac_f32_e32 v154, v192, v192
	v_fmac_f32_e32 v182, v193, v193
	v_add_f32_e32 v154, v154, v182
	v_fmac_f32_e32 v189, 0xba000000, v146
	v_fmac_f32_e32 v187, 0xba000000, v146
	v_add_f32_e32 v148, v154, v148
	v_fmac_f32_e32 v188, 0xba000000, v146
	v_fmac_f32_e32 v186, 0xba000000, v146
	v_mul_f32_e32 v154, v187, v187
	v_mul_f32_e32 v182, v189, v189
	v_fmac_f32_e32 v154, v186, v186
	v_fmac_f32_e32 v182, v188, v188
	v_add_f32_e32 v154, v154, v182
	v_fmac_f32_e32 v183, 0xba000000, v146
	v_fmac_f32_e32 v155, 0xba000000, v146
	v_add_f32_e32 v148, v154, v148
	v_fmac_f32_e32 v185, 0xba000000, v146
	v_fmac_f32_e32 v211, 0xba000000, v146
	v_mul_f32_e32 v154, v155, v155
	v_mul_f32_e32 v182, v183, v183
	v_fmac_f32_e32 v154, v211, v211
	v_fmac_f32_e32 v182, v185, v185
	v_add_f32_e32 v154, v154, v182
	v_fmac_f32_e32 v157, 0xba000000, v146
	v_fmac_f32_e32 v156, 0xba000000, v146
	v_add_f32_e32 v148, v154, v148
	v_fmac_f32_e32 v153, 0xba000000, v146
	v_fmac_f32_e32 v152, 0xba000000, v146
	v_mul_f32_e32 v154, v156, v156
	v_mul_f32_e32 v182, v157, v157
	v_fmac_f32_e32 v154, v152, v152
	v_fmac_f32_e32 v182, v153, v153
	v_add_f32_e32 v154, v154, v182
	v_fmac_f32_e32 v151, 0xba000000, v146
	v_fmac_f32_e32 v145, 0xba000000, v146
	v_add_f32_e32 v148, v154, v148
	v_fmac_f32_e32 v150, 0xba000000, v146
	v_fmac_f32_e32 v144, 0xba000000, v146
	v_mul_f32_e32 v154, v145, v145
	v_mul_f32_e32 v182, v151, v151
	v_fmac_f32_e32 v154, v144, v144
	v_fmac_f32_e32 v182, v150, v150
	v_add_f32_e32 v154, v154, v182
	v_fmac_f32_e32 v147, 0xba000000, v146
	v_fmac_f32_e32 v139, 0xba000000, v146
	v_add_f32_e32 v148, v154, v148
	v_fmac_f32_e32 v149, 0xba000000, v146
	v_fmac_f32_e32 v138, 0xba000000, v146
	v_mul_f32_e32 v154, v139, v139
	v_mul_f32_e32 v182, v147, v147
	v_fmac_f32_e32 v154, v138, v138
	v_fmac_f32_e32 v182, v149, v149
	v_add_f32_e32 v154, v154, v182
	v_add_f32_e32 v148, v154, v148
	s_waitcnt lgkmcnt(0)
	s_nop 1
	v_add_f32_dpp v148, v148, v148 quad_perm:[1,0,3,2] row_mask:0xf bank_mask:0xf
	s_waitcnt lgkmcnt(0)
	s_nop 1
	v_add_f32_dpp v148, v148, v148 quad_perm:[2,3,0,1] row_mask:0xf bank_mask:0xf
	s_waitcnt lgkmcnt(0)
	s_nop 1
	v_add_f32_dpp v148, v148, v148 row_half_mirror row_mask:0xf bank_mask:0xf
	s_waitcnt lgkmcnt(0)
	s_nop 1
	v_add_f32_dpp v148, v148, v148 row_mirror row_mask:0xf bank_mask:0xf
	s_waitcnt lgkmcnt(0)
	v_mov_b32_e32 v154, v148
	s_nop 1
	v_permlane16_swap_b32_e32 v154, v148
	v_add_f32_e32 v148, v148, v154
	s_waitcnt lgkmcnt(0)
	v_mov_b32_e32 v154, v148
	s_nop 1
	v_permlane32_swap_b32_e32 v154, v148
	v_add_f32_e32 v148, v148, v154
	v_fmamk_f32 v148, v148, 0x3a000000, v217
	v_mul_f32_e32 v154, 0x4f800000, v148
	v_cmp_gt_f32_e32 vcc, s87, v148
	s_nop 1
	v_cndmask_b32_e32 v148, v148, v154, vcc
	v_sqrt_f32_e32 v154, v148
	s_nop 0
	v_add_u32_e32 v182, -1, v154
	v_fma_f32 v184, -v182, v154, v148
	v_cmp_ge_f32_e64 s[8:9], 0, v184
	v_add_u32_e32 v184, 1, v154
	s_nop 0
	v_cndmask_b32_e64 v182, v154, v182, s[8:9]
	v_fma_f32 v154, -v184, v154, v148
	v_cmp_lt_f32_e64 s[8:9], 0, v154
	s_nop 1
	v_cndmask_b32_e64 v154, v182, v184, s[8:9]
	v_mul_f32_e32 v182, 0x37800000, v154
	v_cndmask_b32_e32 v154, v154, v182, vcc
	v_cmp_class_f32_e32 vcc, v148, v218
	s_nop 1
	v_cndmask_b32_e32 v148, v154, v148, vcc
	v_div_scale_f32 v154, s[8:9], v148, v148, 1.0
	v_rcp_f32_e32 v182, v154
	s_nop 0
	v_fma_f32 v184, -v154, v182, 1.0
	v_fmac_f32_e32 v182, v184, v182
	v_div_scale_f32 v184, vcc, 1.0, v148, 1.0
	v_mul_f32_e32 v210, v184, v182
	v_fma_f32 v212, -v154, v210, v184
	v_fmac_f32_e32 v210, v212, v182
	v_fma_f32 v154, -v154, v210, v184
	v_div_fmas_f32 v154, v154, v182, v210
	v_div_fixup_f32 v148, v154, v148, 1.0
	s_and_saveexec_b64 s[8:9], s[4:5]
	s_add_i32 s12, s78, 0
	v_mul_f32_e32 v212, 0x3a000000, v146
	v_mov_b32_e32 v213, v148
	v_mov_b32_e32 v146, s12
	ds_write_b64 v146, v[212:213] offset:33792
	s_or_b64 exec, exec, s[8:9]
	s_lshl_b64 s[8:9], s[10:11], 11
	v_mov_b32_e32 v212, v208
	v_mov_b32_e32 v213, v190
	v_mov_b32_e32 v190, v209
	s_lshl_b64 s[8:9], s[8:9], 1
	s_add_u32 s10, s80, s8
	v_mov_b32_e32 v214, v204
	v_mov_b32_e32 v215, v206
	v_pk_mul_f32 v[212:213], v[212:213], v[148:149] op_sel_hi:[1,0]
	v_mov_b32_e32 v206, v205
	v_pk_mul_f32 v[190:191], v[190:191], v[148:149] op_sel_hi:[1,0]
	v_mov_b32_e32 v208, v192
	v_mov_b32_e32 v209, v194
	v_mov_b32_e32 v154, v211
	s_addc_u32 s11, s81, s9
	v_pk_mul_f32 v[214:215], v[214:215], v[148:149] op_sel_hi:[1,0]
	s_waitcnt vmcnt(29)
	v_pk_fma_f32 v[212:213], v[102:103], v[212:213], v[106:107]
	v_pk_mul_f32 v[204:205], v[206:207], v[148:149] op_sel_hi:[1,0]
	s_waitcnt vmcnt(28)
	v_pk_fma_f32 v[190:191], v[94:95], v[190:191], v[98:99]
	v_pk_fma_f32 v[214:215], v[104:105], v[214:215], v[108:109]
	v_cvt_pk_bf16_f32 v212, v212, v213
	v_pk_fma_f32 v[204:205], v[96:97], v[204:205], v[100:101]
	v_cvt_pk_bf16_f32 v213, v214, v215
	global_store_dwordx2 v2, v[212:213], s[10:11]
	v_cvt_pk_bf16_f32 v190, v190, v191
	v_cvt_pk_bf16_f32 v191, v204, v205
	v_mov_b32_e32 v194, v193
	v_pk_mul_f32 v[192:193], v[208:209], v[148:149] op_sel_hi:[1,0]
	v_pk_mul_f32 v[186:187], v[186:187], v[148:149] op_sel_hi:[1,0]
	v_mov_b32_e32 v182, v185
	v_pk_mul_f32 v[154:155], v[154:155], v[148:149] op_sel_hi:[1,0]
	global_store_dwordx2 v2, v[190:191], s[10:11] offset:512
	v_pk_mul_f32 v[190:191], v[194:195], v[148:149] op_sel_hi:[1,0]
	s_waitcnt vmcnt(27)
	v_pk_fma_f32 v[192:193], v[86:87], v[192:193], v[90:91]
	v_pk_mul_f32 v[188:189], v[188:189], v[148:149] op_sel_hi:[1,0]
	s_waitcnt vmcnt(26)
	v_pk_fma_f32 v[186:187], v[78:79], v[186:187], v[82:83]
	v_pk_mul_f32 v[182:183], v[182:183], v[148:149] op_sel_hi:[1,0]
	s_waitcnt vmcnt(24)
	v_pk_fma_f32 v[154:155], v[70:71], v[154:155], v[74:75]
	v_mov_b32_e32 v210, v152
	v_mov_b32_e32 v211, v156
	v_pk_fma_f32 v[190:191], v[88:89], v[190:191], v[92:93]
	v_cvt_pk_bf16_f32 v192, v192, v193
	v_pk_fma_f32 v[188:189], v[80:81], v[188:189], v[84:85]
	v_cvt_pk_bf16_f32 v193, v190, v191
	global_store_dwordx2 v2, v[192:193], s[10:11] offset:1024
	v_cvt_pk_bf16_f32 v186, v186, v187
	v_cvt_pk_bf16_f32 v187, v188, v189
	global_store_dwordx2 v2, v[186:187], s[10:11] offset:1536
	v_pk_fma_f32 v[182:183], v[72:73], v[182:183], v[76:77]
	v_cvt_pk_bf16_f32 v154, v154, v155
	v_mov_b32_e32 v156, v153
	v_cvt_pk_bf16_f32 v155, v182, v183
	global_store_dwordx2 v2, v[154:155], s[10:11] offset:2048
	v_pk_mul_f32 v[154:155], v[210:211], v[148:149] op_sel_hi:[1,0]
	s_waitcnt vmcnt(20)
	v_lshlrev_b32_e32 v211, 16, v132
	s_waitcnt vmcnt(16)
	v_lshlrev_b32_e32 v210, 16, v136
	v_and_b32_e32 v193, 0xffff0000, v132
	v_and_b32_e32 v192, 0xffff0000, v136
	v_lshlrev_b32_e32 v207, 16, v133
	v_lshlrev_b32_e32 v206, 16, v137
	v_and_b32_e32 v209, 0xffff0000, v133
	v_and_b32_e32 v208, 0xffff0000, v137
	v_pk_mul_f32 v[152:153], v[156:157], v[148:149] op_sel_hi:[1,0]
	v_pk_fma_f32 v[154:155], v[62:63], v[154:155], v[66:67]
	v_pk_add_f32 v[132:133], v[210:211], v[192:193]
	v_pk_add_f32 v[136:137], v[206:207], v[208:209]
	v_lshlrev_b32_e32 v195, 16, v129
	v_lshlrev_b32_e32 v194, 16, v128
	v_and_b32_e32 v205, 0xffff0000, v129
	v_and_b32_e32 v204, 0xffff0000, v128
	v_pk_fma_f32 v[152:153], v[64:65], v[152:153], v[68:69]
	v_cvt_pk_bf16_f32 v154, v154, v155
	v_pk_mul_f32 v[144:145], v[144:145], v[148:149] op_sel_hi:[1,0]
	v_cvt_pk_bf16_f32 v155, v152, v153
	v_pk_add_f32 v[132:133], v[132:133], v[136:137]
	v_pk_add_f32 v[128:129], v[194:195], v[204:205]
	global_store_dwordx2 v2, v[154:155], s[10:11] offset:2560
	v_pk_mul_f32 v[150:151], v[150:151], v[148:149] op_sel_hi:[1,0]
	v_pk_fma_f32 v[144:145], v[54:55], v[144:145], v[58:59]
	v_add_f32_e32 v132, 0, v132
	v_lshlrev_b32_e32 v188, 16, v124
	v_and_b32_e32 v189, 0xffff0000, v124
	v_lshlrev_b32_e32 v190, 16, v125
	v_and_b32_e32 v191, 0xffff0000, v125
	v_lshlrev_b32_e32 v213, 16, v120
	v_and_b32_e32 v183, 0xffff0000, v120
	v_lshlrev_b32_e32 v157, 16, v121
	v_and_b32_e32 v155, 0xffff0000, v121
	v_pk_add_f32 v[120:121], v[128:129], v[128:129] op_sel:[0,1] op_sel_hi:[1,0]
	v_pk_fma_f32 v[150:151], v[56:57], v[150:151], v[60:61]
	v_cvt_pk_bf16_f32 v144, v144, v145
	v_mov_b32_e32 v146, v149
	v_cvt_pk_bf16_f32 v145, v150, v151
	v_add_f32_e32 v212, v132, v133
	v_add_f32_e32 v156, v188, v189
	v_add_f32_e32 v154, v190, v191
	v_mov_b32_e32 v121, v183
	global_store_dwordx2 v2, v[144:145], s[10:11] offset:3072
	v_pk_mul_f32 v[144:145], v[146:147], v[148:149] op_sel_hi:[1,0]
	v_pk_mul_f32 v[138:139], v[138:139], v[148:149] op_sel_hi:[1,0]
	v_pk_add_f32 v[120:121], v[212:213], v[120:121]
	v_pk_add_f32 v[124:125], v[156:157], v[154:155]
	s_waitcnt vmcnt(17)
	v_lshlrev_b32_e32 v185, 16, v117
	v_lshlrev_b32_e32 v184, 16, v116
	v_and_b32_e32 v187, 0xffff0000, v117
	v_and_b32_e32 v186, 0xffff0000, v116
	v_pk_fma_f32 v[144:145], v[48:49], v[144:145], v[52:53]
	v_pk_fma_f32 v[138:139], v[46:47], v[138:139], v[50:51]
	v_pk_add_f32 v[120:121], v[120:121], v[124:125]
	v_pk_add_f32 v[116:117], v[184:185], v[186:187]
	v_cvt_pk_bf16_f32 v138, v138, v139
	v_cvt_pk_bf16_f32 v139, v144, v145
	s_waitcnt vmcnt(16)
	v_lshlrev_b32_e32 v150, 16, v112
	v_and_b32_e32 v151, 0xffff0000, v112
	v_lshlrev_b32_e32 v152, 16, v113
	v_and_b32_e32 v153, 0xffff0000, v113
	s_waitcnt vmcnt(15)
	v_lshlrev_b32_e32 v148, 16, v4
	v_and_b32_e32 v149, 0xffff0000, v4
	v_lshlrev_b32_e32 v147, 16, v5
	v_and_b32_e32 v145, 0xffff0000, v5
	v_pk_add_f32 v[4:5], v[120:121], v[120:121] op_sel:[0,1] op_sel_hi:[1,0]
	v_pk_add_f32 v[112:113], v[116:117], v[116:117] op_sel:[0,1] op_sel_hi:[1,0]
	v_add_f32_e32 v146, v150, v151
	v_add_f32_e32 v144, v152, v153
	v_mov_b32_e32 v5, v148
	v_mov_b32_e32 v113, v149
	v_pk_add_f32 v[4:5], v[4:5], v[112:113]
	v_pk_add_f32 v[112:113], v[146:147], v[144:145]
	s_movk_i32 s8, 0x3000
	v_pk_add_f32 v[4:5], v[4:5], v[112:113]
	global_store_dwordx2 v2, v[138:139], s[10:11] offset:3584
	v_add_f32_e32 v144, v4, v5
	v_add_co_u32_e32 v4, vcc, s8, v110
	s_nop 1
	v_addc_co_u32_e32 v5, vcc, 0, v111, vcc
	global_load_dwordx2 v[136:137], v[4:5], off
	global_load_dwordx2 v[138:139], v[4:5], off offset:512
	global_load_dwordx2 v[132:133], v[4:5], off offset:1024
	global_load_dwordx2 v[128:129], v[4:5], off offset:1536
	global_load_dwordx2 v[124:125], v[4:5], off offset:2048
	global_load_dwordx2 v[120:121], v[4:5], off offset:2560
	global_load_dwordx2 v[116:117], v[4:5], off offset:3072
	global_load_dwordx2 v[112:113], v[4:5], off offset:3584
	s_waitcnt lgkmcnt(0)
	s_nop 1
	v_add_f32_dpp v4, v144, v144 quad_perm:[1,0,3,2] row_mask:0xf bank_mask:0xf
	s_waitcnt lgkmcnt(0)
	s_nop 1
	v_add_f32_dpp v4, v4, v4 quad_perm:[2,3,0,1] row_mask:0xf bank_mask:0xf
	s_waitcnt lgkmcnt(0)
	s_nop 1
	v_add_f32_dpp v4, v4, v4 row_half_mirror row_mask:0xf bank_mask:0xf
	s_waitcnt lgkmcnt(0)
	s_nop 1
	v_add_f32_dpp v4, v4, v4 row_mirror row_mask:0xf bank_mask:0xf
	s_waitcnt lgkmcnt(0)
	v_mov_b32_e32 v5, v4
	s_nop 1
	v_permlane16_swap_b32_e32 v5, v4
	v_add_f32_e32 v4, v4, v5
	s_waitcnt lgkmcnt(0)
	v_mov_b32_e32 v5, v4
	s_nop 1
	v_permlane32_swap_b32_e32 v5, v4
	v_add_f32_e32 v4, v4, v5
	v_fmac_f32_e32 v208, 0xba000000, v4
	v_fmac_f32_e32 v192, 0xba000000, v4
	v_fmac_f32_e32 v206, 0xba000000, v4
	v_fmac_f32_e32 v210, 0xba000000, v4
	v_mul_f32_e32 v5, v192, v192
	v_mul_f32_e32 v144, v208, v208
	v_fmac_f32_e32 v5, v210, v210
	v_fmac_f32_e32 v144, v206, v206
	v_fmac_f32_e32 v209, 0xba000000, v4
	v_fmac_f32_e32 v193, 0xba000000, v4
	v_add_f32_e32 v5, v5, v144
	v_fmac_f32_e32 v207, 0xba000000, v4
	v_fmac_f32_e32 v211, 0xba000000, v4
	v_mul_f32_e32 v144, v193, v193
	v_mul_f32_e32 v146, v209, v209
	v_fmac_f32_e32 v144, v211, v211
	v_fmac_f32_e32 v146, v207, v207
	v_add_f32_e32 v144, v144, v146
	v_fmac_f32_e32 v205, 0xba000000, v4
	v_fmac_f32_e32 v204, 0xba000000, v4
	v_add_f32_e32 v5, v5, v144
	v_fmac_f32_e32 v195, 0xba000000, v4
	v_fmac_f32_e32 v194, 0xba000000, v4
	v_mul_f32_e32 v144, v204, v204
	v_mul_f32_e32 v146, v205, v205
	v_fmac_f32_e32 v144, v194, v194
	v_fmac_f32_e32 v146, v195, v195
	v_add_f32_e32 v144, v144, v146
	v_fmac_f32_e32 v191, 0xba000000, v4
	v_fmac_f32_e32 v189, 0xba000000, v4
	v_add_f32_e32 v5, v144, v5
	v_fmac_f32_e32 v190, 0xba000000, v4
	v_fmac_f32_e32 v188, 0xba000000, v4
	v_mul_f32_e32 v144, v189, v189
	v_mul_f32_e32 v146, v191, v191
	v_fmac_f32_e32 v144, v188, v188
	v_fmac_f32_e32 v146, v190, v190
	v_add_f32_e32 v144, v144, v146
	v_fmac_f32_e32 v155, 0xba000000, v4
	v_fmac_f32_e32 v183, 0xba000000, v4
	v_add_f32_e32 v5, v144, v5
	v_fmac_f32_e32 v157, 0xba000000, v4
	v_fmac_f32_e32 v213, 0xba000000, v4
	v_mul_f32_e32 v144, v183, v183
	v_mul_f32_e32 v146, v155, v155
	v_fmac_f32_e32 v144, v213, v213
	v_fmac_f32_e32 v146, v157, v157
	v_add_f32_e32 v144, v144, v146
	v_fmac_f32_e32 v187, 0xba000000, v4
	v_fmac_f32_e32 v186, 0xba000000, v4
	v_add_f32_e32 v5, v144, v5
	v_fmac_f32_e32 v185, 0xba000000, v4
	v_fmac_f32_e32 v184, 0xba000000, v4
	v_mul_f32_e32 v144, v186, v186
	v_mul_f32_e32 v146, v187, v187
	v_fmac_f32_e32 v144, v184, v184
	v_fmac_f32_e32 v146, v185, v185
	v_add_f32_e32 v144, v144, v146
	v_fmac_f32_e32 v153, 0xba000000, v4
	v_fmac_f32_e32 v151, 0xba000000, v4
	v_add_f32_e32 v5, v144, v5
	v_fmac_f32_e32 v152, 0xba000000, v4
	v_fmac_f32_e32 v150, 0xba000000, v4
	v_mul_f32_e32 v144, v151, v151
	v_mul_f32_e32 v146, v153, v153
	v_fmac_f32_e32 v144, v150, v150
	v_fmac_f32_e32 v146, v152, v152
	v_add_f32_e32 v144, v144, v146
	v_fmac_f32_e32 v145, 0xba000000, v4
	v_fmac_f32_e32 v149, 0xba000000, v4
	v_add_f32_e32 v5, v144, v5
	v_fmac_f32_e32 v147, 0xba000000, v4
	v_fmac_f32_e32 v148, 0xba000000, v4
	v_mul_f32_e32 v144, v149, v149
	v_mul_f32_e32 v146, v145, v145
	v_fmac_f32_e32 v144, v148, v148
	v_fmac_f32_e32 v146, v147, v147
	v_add_f32_e32 v144, v144, v146
	v_add_f32_e32 v5, v144, v5
	s_waitcnt lgkmcnt(0)
	s_nop 1
	v_add_f32_dpp v5, v5, v5 quad_perm:[1,0,3,2] row_mask:0xf bank_mask:0xf
	s_waitcnt lgkmcnt(0)
	s_nop 1
	v_add_f32_dpp v5, v5, v5 quad_perm:[2,3,0,1] row_mask:0xf bank_mask:0xf
	s_waitcnt lgkmcnt(0)
	s_nop 1
	v_add_f32_dpp v5, v5, v5 row_half_mirror row_mask:0xf bank_mask:0xf
	s_waitcnt lgkmcnt(0)
	s_nop 1
	v_add_f32_dpp v5, v5, v5 row_mirror row_mask:0xf bank_mask:0xf
	s_waitcnt lgkmcnt(0)
	v_mov_b32_e32 v144, v5
	s_nop 1
	v_permlane16_swap_b32_e32 v144, v5
	v_add_f32_e32 v5, v5, v144
	s_waitcnt lgkmcnt(0)
	v_mov_b32_e32 v144, v5
	s_nop 1
	v_permlane32_swap_b32_e32 v144, v5
	v_add_f32_e32 v5, v5, v144
	v_fmamk_f32 v5, v5, 0x3a000000, v217
	v_cmp_gt_f32_e32 vcc, s87, v5
	v_mul_f32_e32 v144, 0x4f800000, v5
	s_nop 0
	v_cndmask_b32_e32 v5, v5, v144, vcc
	v_sqrt_f32_e32 v144, v5
	s_nop 0
	v_add_u32_e32 v146, -1, v144
	v_fma_f32 v154, -v146, v144, v5
	v_cmp_ge_f32_e64 s[8:9], 0, v154
	v_add_u32_e32 v154, 1, v144
	s_nop 0
	v_cndmask_b32_e64 v146, v144, v146, s[8:9]
	v_fma_f32 v144, -v154, v144, v5
	v_cmp_lt_f32_e64 s[8:9], 0, v144
	s_nop 1
	v_cndmask_b32_e64 v144, v146, v154, s[8:9]
	v_mul_f32_e32 v146, 0x37800000, v144
	v_cndmask_b32_e32 v144, v144, v146, vcc
	v_cmp_class_f32_e32 vcc, v5, v218
	s_nop 1
	v_cndmask_b32_e32 v5, v144, v5, vcc
	v_div_scale_f32 v144, s[8:9], v5, v5, 1.0
	v_rcp_f32_e32 v146, v144
	s_nop 0
	v_fma_f32 v154, -v144, v146, 1.0
	v_fmac_f32_e32 v146, v154, v146
	v_div_scale_f32 v154, vcc, 1.0, v5, 1.0
	v_mul_f32_e32 v156, v154, v146
	v_fma_f32 v182, -v144, v156, v154
	v_fmac_f32_e32 v156, v182, v146
	v_fma_f32 v144, -v144, v156, v154
	v_div_fmas_f32 v144, v144, v146, v156
	v_div_fixup_f32 v146, v144, v5, 1.0
	s_and_saveexec_b64 s[8:9], s[4:5]
	s_add_i32 s12, s78, 0
	v_mul_f32_e32 v4, 0x3a000000, v4
	v_mov_b32_e32 v5, v146
	v_mov_b32_e32 v144, s12
	ds_write_b64 v144, v[4:5] offset:33800
	s_or_b64 exec, exec, s[8:9]
	v_mov_b32_e32 v214, v210
	v_mov_b32_e32 v215, v192
	v_mov_b32_e32 v240, v206
	v_mov_b32_e32 v241, v208
	v_pk_mul_f32 v[240:241], v[240:241], v[146:147] op_sel_hi:[1,0]
	v_pk_mul_f32 v[214:215], v[214:215], v[146:147] op_sel_hi:[1,0]
	v_lshl_add_u64 v[4:5], s[10:11], 0, v[2:3]
	v_mov_b32_e32 v192, v211
	v_pk_fma_f32 v[240:241], v[104:105], v[240:241], v[108:109]
	v_pk_fma_f32 v[214:215], v[102:103], v[214:215], v[106:107]
	s_movk_i32 s8, 0x1000
	v_cvt_pk_bf16_f32 v214, v214, v215
	v_cvt_pk_bf16_f32 v215, v240, v241
	v_add_co_u32_e32 v240, vcc, s8, v4
	v_mov_b32_e32 v208, v207
	v_pk_mul_f32 v[192:193], v[192:193], v[146:147] op_sel_hi:[1,0]
	v_addc_co_u32_e32 v241, vcc, 0, v5, vcc
	v_pk_mul_f32 v[206:207], v[208:209], v[146:147] op_sel_hi:[1,0]
	v_pk_fma_f32 v[192:193], v[94:95], v[192:193], v[98:99]
	v_mov_b32_e32 v210, v194
	v_mov_b32_e32 v211, v204
	v_mov_b32_e32 v182, v213
	global_store_dwordx2 v[240:241], v[214:215], off
	v_pk_fma_f32 v[206:207], v[96:97], v[206:207], v[100:101]
	v_cvt_pk_bf16_f32 v192, v192, v193
	v_mov_b32_e32 v204, v195
	v_cvt_pk_bf16_f32 v193, v206, v207
	global_store_dwordx2 v[240:241], v[192:193], off offset:512
	v_pk_mul_f32 v[192:193], v[204:205], v[146:147] op_sel_hi:[1,0]
	v_pk_mul_f32 v[194:195], v[210:211], v[146:147] op_sel_hi:[1,0]
	v_pk_mul_f32 v[188:189], v[188:189], v[146:147] op_sel_hi:[1,0]
	v_mov_b32_e32 v154, v157
	v_pk_mul_f32 v[156:157], v[182:183], v[146:147] op_sel_hi:[1,0]
	v_pk_fma_f32 v[192:193], v[88:89], v[192:193], v[92:93]
	v_pk_fma_f32 v[194:195], v[86:87], v[194:195], v[90:91]
	v_pk_mul_f32 v[190:191], v[190:191], v[146:147] op_sel_hi:[1,0]
	v_pk_fma_f32 v[188:189], v[78:79], v[188:189], v[82:83]
	v_pk_mul_f32 v[154:155], v[154:155], v[146:147] op_sel_hi:[1,0]
	v_pk_fma_f32 v[156:157], v[70:71], v[156:157], v[74:75]
	v_mov_b32_e32 v212, v184
	v_mov_b32_e32 v213, v186
	v_cvt_pk_bf16_f32 v194, v194, v195
	v_cvt_pk_bf16_f32 v195, v192, v193
	global_store_dwordx2 v[240:241], v[194:195], off offset:1024
	v_pk_fma_f32 v[190:191], v[80:81], v[190:191], v[84:85]
	v_cvt_pk_bf16_f32 v188, v188, v189
	v_pk_fma_f32 v[154:155], v[72:73], v[154:155], v[76:77]
	v_cvt_pk_bf16_f32 v189, v190, v191
	global_store_dwordx2 v[240:241], v[188:189], off offset:1536
	v_cvt_pk_bf16_f32 v156, v156, v157
	v_cvt_pk_bf16_f32 v157, v154, v155
	v_mov_b32_e32 v186, v185
	s_waitcnt vmcnt(26)
	v_lshlrev_b32_e32 v211, 16, v142
	v_lshlrev_b32_e32 v210, 16, v140
	v_and_b32_e32 v193, 0xffff0000, v142
	v_and_b32_e32 v192, 0xffff0000, v140
	v_lshlrev_b32_e32 v207, 16, v143
	v_lshlrev_b32_e32 v206, 16, v141
	v_and_b32_e32 v209, 0xffff0000, v143
	v_and_b32_e32 v208, 0xffff0000, v141
	global_store_dwordx2 v[240:241], v[156:157], off offset:2048
	v_pk_mul_f32 v[154:155], v[186:187], v[146:147] op_sel_hi:[1,0]
	v_pk_mul_f32 v[156:157], v[212:213], v[146:147] op_sel_hi:[1,0]
	v_pk_add_f32 v[140:141], v[210:211], v[192:193]
	v_pk_add_f32 v[142:143], v[206:207], v[208:209]
	s_waitcnt vmcnt(26)
	v_lshlrev_b32_e32 v195, 16, v135
	v_lshlrev_b32_e32 v194, 16, v134
	v_and_b32_e32 v205, 0xffff0000, v135
	v_and_b32_e32 v204, 0xffff0000, v134
	v_pk_fma_f32 v[154:155], v[64:65], v[154:155], v[68:69]
	v_pk_fma_f32 v[156:157], v[62:63], v[156:157], v[66:67]
	v_pk_add_f32 v[140:141], v[140:141], v[142:143]
	v_pk_add_f32 v[134:135], v[194:195], v[204:205]
	v_cvt_pk_bf16_f32 v156, v156, v157
	v_cvt_pk_bf16_f32 v157, v154, v155
	v_mov_b32_e32 v144, v147
	v_add_f32_e32 v2, 0, v140
	s_waitcnt vmcnt(25)
	v_lshlrev_b32_e32 v188, 16, v130
	v_and_b32_e32 v189, 0xffff0000, v130
	v_lshlrev_b32_e32 v190, 16, v131
	v_and_b32_e32 v191, 0xffff0000, v131
	s_waitcnt vmcnt(24)
	v_lshlrev_b32_e32 v213, 16, v126
	v_and_b32_e32 v185, 0xffff0000, v126
	v_lshlrev_b32_e32 v183, 16, v127
	v_and_b32_e32 v155, 0xffff0000, v127
	v_pk_add_f32 v[126:127], v[134:135], v[134:135] op_sel:[0,1] op_sel_hi:[1,0]
	v_pk_mul_f32 v[152:153], v[152:153], v[146:147] op_sel_hi:[1,0]
	v_pk_mul_f32 v[150:151], v[150:151], v[146:147] op_sel_hi:[1,0]
	v_pk_mul_f32 v[144:145], v[144:145], v[146:147] op_sel_hi:[1,0]
	v_pk_mul_f32 v[146:147], v[148:149], v[146:147] op_sel_hi:[1,0]
	v_add_f32_e32 v212, v2, v141
	v_add_f32_e32 v182, v188, v189
	v_add_f32_e32 v154, v190, v191
	v_mov_b32_e32 v127, v185
	global_store_dwordx2 v[240:241], v[156:157], off offset:2560
	v_pk_fma_f32 v[150:151], v[54:55], v[150:151], v[58:59]
	v_pk_fma_f32 v[146:147], v[46:47], v[146:147], v[50:51]
	v_pk_add_f32 v[126:127], v[212:213], v[126:127]
	v_pk_add_f32 v[130:131], v[182:183], v[154:155]
	s_waitcnt vmcnt(24)
	v_lshlrev_b32_e32 v157, 16, v123
	v_lshlrev_b32_e32 v156, 16, v122
	v_and_b32_e32 v187, 0xffff0000, v123
	v_and_b32_e32 v186, 0xffff0000, v122
	v_pk_fma_f32 v[152:153], v[56:57], v[152:153], v[60:61]
	v_cvt_pk_bf16_f32 v150, v150, v151
	v_pk_fma_f32 v[144:145], v[48:49], v[144:145], v[52:53]
	v_cvt_pk_bf16_f32 v151, v152, v153
	global_store_dwordx2 v[240:241], v[150:151], off offset:3072
	v_cvt_pk_bf16_f32 v146, v146, v147
	v_cvt_pk_bf16_f32 v147, v144, v145
	v_pk_add_f32 v[126:127], v[126:127], v[130:131]
	v_pk_add_f32 v[122:123], v[156:157], v[186:187]
	global_store_dwordx2 v[240:241], v[146:147], off offset:3584
	s_waitcnt vmcnt(25)
	v_lshlrev_b32_e32 v148, 16, v118
	v_and_b32_e32 v149, 0xffff0000, v118
	v_lshlrev_b32_e32 v152, 16, v119
	v_and_b32_e32 v153, 0xffff0000, v119
	s_waitcnt vmcnt(24)
	v_lshlrev_b32_e32 v146, 16, v114
	v_and_b32_e32 v147, 0xffff0000, v114
	v_lshlrev_b32_e32 v145, 16, v115
	v_and_b32_e32 v143, 0xffff0000, v115
	v_pk_add_f32 v[114:115], v[126:127], v[126:127] op_sel:[0,1] op_sel_hi:[1,0]
	v_pk_add_f32 v[118:119], v[122:123], v[122:123] op_sel:[0,1] op_sel_hi:[1,0]
	v_add_f32_e32 v144, v148, v149
	v_add_f32_e32 v142, v152, v153
	v_mov_b32_e32 v115, v146
	v_mov_b32_e32 v119, v147
	v_pk_add_f32 v[114:115], v[114:115], v[118:119]
	v_pk_add_f32 v[118:119], v[144:145], v[142:143]
	s_movk_i32 s8, 0x4000
	v_pk_add_f32 v[114:115], v[114:115], v[118:119]
	s_nop 0
	v_add_f32_e32 v2, v114, v115
	v_add_co_u32_e32 v114, vcc, s8, v110
	s_waitcnt lgkmcnt(0)
	s_nop 1
	v_add_f32_dpp v2, v2, v2 quad_perm:[1,0,3,2] row_mask:0xf bank_mask:0xf
	v_addc_co_u32_e32 v115, vcc, 0, v111, vcc
	global_load_dwordx2 v[140:141], v[114:115], off
	global_load_dwordx2 v[150:151], v[114:115], off offset:512
	global_load_dwordx2 v[134:135], v[114:115], off offset:1024
	global_load_dwordx2 v[130:131], v[114:115], off offset:1536
	global_load_dwordx2 v[126:127], v[114:115], off offset:2048
	global_load_dwordx2 v[122:123], v[114:115], off offset:2560
	global_load_dwordx2 v[118:119], v[114:115], off offset:3072
	s_nop 0
	global_load_dwordx2 v[114:115], v[114:115], off offset:3584
	s_waitcnt lgkmcnt(0)
	s_nop 1
	v_add_f32_dpp v2, v2, v2 quad_perm:[2,3,0,1] row_mask:0xf bank_mask:0xf
	s_waitcnt lgkmcnt(0)
	s_nop 1
	v_add_f32_dpp v2, v2, v2 row_half_mirror row_mask:0xf bank_mask:0xf
	s_waitcnt lgkmcnt(0)
	s_nop 1
	v_add_f32_dpp v2, v2, v2 row_mirror row_mask:0xf bank_mask:0xf
	s_waitcnt lgkmcnt(0)
	v_mov_b32_e32 v142, v2
	s_nop 1
	v_permlane16_swap_b32_e32 v142, v2
	v_add_f32_e32 v2, v2, v142
	s_waitcnt lgkmcnt(0)
	v_mov_b32_e32 v142, v2
	s_nop 1
	v_permlane32_swap_b32_e32 v142, v2
	v_add_f32_e32 v142, v2, v142
	v_fmac_f32_e32 v208, 0xba000000, v142
	v_fmac_f32_e32 v192, 0xba000000, v142
	v_fmac_f32_e32 v206, 0xba000000, v142
	v_fmac_f32_e32 v210, 0xba000000, v142
	v_mul_f32_e32 v2, v192, v192
	v_mul_f32_e32 v144, v208, v208
	v_fmac_f32_e32 v2, v210, v210
	v_fmac_f32_e32 v144, v206, v206
	v_fmac_f32_e32 v209, 0xba000000, v142
	v_fmac_f32_e32 v193, 0xba000000, v142
	v_add_f32_e32 v2, v2, v144
	v_fmac_f32_e32 v207, 0xba000000, v142
	v_fmac_f32_e32 v211, 0xba000000, v142
	v_mul_f32_e32 v144, v193, v193
	v_mul_f32_e32 v154, v209, v209
	v_fmac_f32_e32 v144, v211, v211
	v_fmac_f32_e32 v154, v207, v207
	v_add_f32_e32 v144, v144, v154
	v_fmac_f32_e32 v205, 0xba000000, v142
	v_fmac_f32_e32 v204, 0xba000000, v142
	v_add_f32_e32 v2, v2, v144
	v_fmac_f32_e32 v195, 0xba000000, v142
	v_fmac_f32_e32 v194, 0xba000000, v142
	v_mul_f32_e32 v144, v204, v204
	v_mul_f32_e32 v154, v205, v205
	v_fmac_f32_e32 v144, v194, v194
	v_fmac_f32_e32 v154, v195, v195
	v_add_f32_e32 v144, v144, v154
	v_fmac_f32_e32 v191, 0xba000000, v142
	v_fmac_f32_e32 v189, 0xba000000, v142
	v_add_f32_e32 v2, v144, v2
	v_fmac_f32_e32 v190, 0xba000000, v142
	v_fmac_f32_e32 v188, 0xba000000, v142
	v_mul_f32_e32 v144, v189, v189
	v_mul_f32_e32 v154, v191, v191
	v_fmac_f32_e32 v144, v188, v188
	v_fmac_f32_e32 v154, v190, v190
	v_add_f32_e32 v144, v144, v154
	v_fmac_f32_e32 v155, 0xba000000, v142
	v_fmac_f32_e32 v185, 0xba000000, v142
	v_add_f32_e32 v2, v144, v2
	v_fmac_f32_e32 v183, 0xba000000, v142
	v_fmac_f32_e32 v213, 0xba000000, v142
	v_mul_f32_e32 v144, v185, v185
	v_mul_f32_e32 v154, v155, v155
	v_fmac_f32_e32 v144, v213, v213
	v_fmac_f32_e32 v154, v183, v183
	v_add_f32_e32 v144, v144, v154
	v_fmac_f32_e32 v187, 0xba000000, v142
	v_fmac_f32_e32 v186, 0xba000000, v142
	v_add_f32_e32 v2, v144, v2
	v_fmac_f32_e32 v157, 0xba000000, v142
	v_fmac_f32_e32 v156, 0xba000000, v142
	v_mul_f32_e32 v144, v186, v186
	v_mul_f32_e32 v154, v187, v187
	v_fmac_f32_e32 v144, v156, v156
	v_fmac_f32_e32 v154, v157, v157
	v_add_f32_e32 v144, v144, v154
	v_fmac_f32_e32 v153, 0xba000000, v142
	v_fmac_f32_e32 v149, 0xba000000, v142
	v_add_f32_e32 v2, v144, v2
	v_fmac_f32_e32 v152, 0xba000000, v142
	v_fmac_f32_e32 v148, 0xba000000, v142
	v_mul_f32_e32 v144, v149, v149
	v_mul_f32_e32 v154, v153, v153
	v_fmac_f32_e32 v144, v148, v148
	v_fmac_f32_e32 v154, v152, v152
	v_add_f32_e32 v144, v144, v154
	v_fmac_f32_e32 v143, 0xba000000, v142
	v_fmac_f32_e32 v147, 0xba000000, v142
	v_add_f32_e32 v2, v144, v2
	v_fmac_f32_e32 v145, 0xba000000, v142
	v_fmac_f32_e32 v146, 0xba000000, v142
	v_mul_f32_e32 v144, v147, v147
	v_mul_f32_e32 v154, v143, v143
	v_fmac_f32_e32 v144, v146, v146
	v_fmac_f32_e32 v154, v145, v145
	v_add_f32_e32 v144, v144, v154
	v_add_f32_e32 v2, v144, v2
	s_waitcnt lgkmcnt(0)
	s_nop 1
	v_add_f32_dpp v2, v2, v2 quad_perm:[1,0,3,2] row_mask:0xf bank_mask:0xf
	s_waitcnt lgkmcnt(0)
	s_nop 1
	v_add_f32_dpp v2, v2, v2 quad_perm:[2,3,0,1] row_mask:0xf bank_mask:0xf
	s_waitcnt lgkmcnt(0)
	s_nop 1
	v_add_f32_dpp v2, v2, v2 row_half_mirror row_mask:0xf bank_mask:0xf
	s_waitcnt lgkmcnt(0)
	s_nop 1
	v_add_f32_dpp v2, v2, v2 row_mirror row_mask:0xf bank_mask:0xf
	s_waitcnt lgkmcnt(0)
	v_mov_b32_e32 v144, v2
	s_nop 1
	v_permlane16_swap_b32_e32 v144, v2
	v_add_f32_e32 v2, v2, v144
	s_waitcnt lgkmcnt(0)
	v_mov_b32_e32 v144, v2
	s_nop 1
	v_permlane32_swap_b32_e32 v144, v2
	v_add_f32_e32 v2, v2, v144
	v_fmamk_f32 v2, v2, 0x3a000000, v217
	v_cmp_gt_f32_e32 vcc, s87, v2
	v_mul_f32_e32 v144, 0x4f800000, v2
	s_nop 0
	v_cndmask_b32_e32 v2, v2, v144, vcc
	v_sqrt_f32_e32 v144, v2
	s_nop 0
	v_add_u32_e32 v154, -1, v144
	v_fma_f32 v182, -v154, v144, v2
	v_cmp_ge_f32_e64 s[8:9], 0, v182
	v_add_u32_e32 v182, 1, v144
	s_nop 0
	v_cndmask_b32_e64 v154, v144, v154, s[8:9]
	v_fma_f32 v144, -v182, v144, v2
	v_cmp_lt_f32_e64 s[8:9], 0, v144
	s_nop 1
	v_cndmask_b32_e64 v144, v154, v182, s[8:9]
	v_mul_f32_e32 v154, 0x37800000, v144
	v_cndmask_b32_e32 v144, v144, v154, vcc
	v_cmp_class_f32_e32 vcc, v2, v218
	s_nop 1
	v_cndmask_b32_e32 v2, v144, v2, vcc
	v_div_scale_f32 v144, s[8:9], v2, v2, 1.0
	v_rcp_f32_e32 v154, v144
	s_nop 0
	v_fma_f32 v182, -v144, v154, 1.0
	v_fmac_f32_e32 v154, v182, v154
	v_div_scale_f32 v182, vcc, 1.0, v2, 1.0
	v_mul_f32_e32 v184, v182, v154
	v_fma_f32 v212, -v144, v184, v182
	v_fmac_f32_e32 v184, v212, v154
	v_fma_f32 v144, -v144, v184, v182
	v_div_fmas_f32 v144, v144, v154, v184
	v_div_fixup_f32 v2, v144, v2, 1.0
	s_and_saveexec_b64 s[8:9], s[4:5]
	s_add_i32 s10, s78, 0
	v_mul_f32_e32 v214, 0x3a000000, v142
	v_mov_b32_e32 v215, v2
	v_mov_b32_e32 v142, s10
	ds_write_b64 v142, v[214:215] offset:33808
	s_or_b64 exec, exec, s[8:9]
	v_mov_b32_e32 v214, v210
	v_mov_b32_e32 v215, v192
	v_mov_b32_e32 v240, v206
	v_mov_b32_e32 v241, v208
	v_pk_mul_f32 v[240:241], v[240:241], v[2:3] op_sel_hi:[1,0]
	v_pk_mul_f32 v[214:215], v[214:215], v[2:3] op_sel_hi:[1,0]
	v_mov_b32_e32 v192, v211
	v_pk_fma_f32 v[240:241], v[104:105], v[240:241], v[108:109]
	v_pk_fma_f32 v[214:215], v[102:103], v[214:215], v[106:107]
	v_mov_b32_e32 v208, v207
	v_cvt_pk_bf16_f32 v214, v214, v215
	v_cvt_pk_bf16_f32 v215, v240, v241
	v_add_co_u32_e32 v240, vcc, s89, v4
	v_pk_mul_f32 v[192:193], v[192:193], v[2:3] op_sel_hi:[1,0]
	s_nop 0
	v_addc_co_u32_e32 v241, vcc, 0, v5, vcc
	v_pk_mul_f32 v[206:207], v[208:209], v[2:3] op_sel_hi:[1,0]
	v_pk_fma_f32 v[192:193], v[94:95], v[192:193], v[98:99]
	v_mov_b32_e32 v210, v194
	v_mov_b32_e32 v211, v204
	global_store_dwordx2 v[240:241], v[214:215], off
	v_pk_fma_f32 v[206:207], v[96:97], v[206:207], v[100:101]
	v_cvt_pk_bf16_f32 v192, v192, v193
	v_mov_b32_e32 v204, v195
	v_cvt_pk_bf16_f32 v193, v206, v207
	v_mov_b32_e32 v184, v213
	global_store_dwordx2 v[240:241], v[192:193], off offset:512
	v_pk_mul_f32 v[192:193], v[204:205], v[2:3] op_sel_hi:[1,0]
	v_pk_mul_f32 v[194:195], v[210:211], v[2:3] op_sel_hi:[1,0]
	v_mov_b32_e32 v154, v183
	v_mov_b32_e32 v212, v156
	v_mov_b32_e32 v213, v186
	v_pk_fma_f32 v[192:193], v[88:89], v[192:193], v[92:93]
	v_pk_fma_f32 v[194:195], v[86:87], v[194:195], v[90:91]
	v_pk_mul_f32 v[188:189], v[188:189], v[2:3] op_sel_hi:[1,0]
	v_pk_mul_f32 v[154:155], v[154:155], v[2:3] op_sel_hi:[1,0]
	v_pk_mul_f32 v[182:183], v[184:185], v[2:3] op_sel_hi:[1,0]
	v_cvt_pk_bf16_f32 v194, v194, v195
	v_cvt_pk_bf16_f32 v195, v192, v193
	v_pk_mul_f32 v[190:191], v[190:191], v[2:3] op_sel_hi:[1,0]
	v_pk_fma_f32 v[188:189], v[78:79], v[188:189], v[82:83]
	v_pk_fma_f32 v[154:155], v[72:73], v[154:155], v[76:77]
	v_pk_fma_f32 v[182:183], v[70:71], v[182:183], v[74:75]
	v_mov_b32_e32 v186, v157
	v_pk_mul_f32 v[156:157], v[212:213], v[2:3] op_sel_hi:[1,0]
	s_waitcnt vmcnt(24)
	v_lshlrev_b32_e32 v211, 16, v138
	v_lshlrev_b32_e32 v210, 16, v136
	v_and_b32_e32 v193, 0xffff0000, v138
	v_and_b32_e32 v192, 0xffff0000, v136
	v_lshlrev_b32_e32 v207, 16, v139
	v_lshlrev_b32_e32 v206, 16, v137
	v_and_b32_e32 v209, 0xffff0000, v139
	v_and_b32_e32 v208, 0xffff0000, v137
	global_store_dwordx2 v[240:241], v[194:195], off offset:1024
	v_pk_fma_f32 v[190:191], v[80:81], v[190:191], v[84:85]
	v_cvt_pk_bf16_f32 v188, v188, v189
	v_pk_fma_f32 v[156:157], v[62:63], v[156:157], v[66:67]
	v_cvt_pk_bf16_f32 v189, v190, v191
	global_store_dwordx2 v[240:241], v[188:189], off offset:1536
	v_cvt_pk_bf16_f32 v182, v182, v183
	v_cvt_pk_bf16_f32 v183, v154, v155
	v_pk_mul_f32 v[154:155], v[186:187], v[2:3] op_sel_hi:[1,0]
	v_pk_add_f32 v[136:137], v[210:211], v[192:193]
	v_pk_add_f32 v[138:139], v[206:207], v[208:209]
	s_waitcnt vmcnt(25)
	v_lshlrev_b32_e32 v195, 16, v133
	v_lshlrev_b32_e32 v194, 16, v132
	v_and_b32_e32 v205, 0xffff0000, v133
	v_and_b32_e32 v204, 0xffff0000, v132
	global_store_dwordx2 v[240:241], v[182:183], off offset:2048
	v_pk_fma_f32 v[154:155], v[64:65], v[154:155], v[68:69]
	v_cvt_pk_bf16_f32 v156, v156, v157
	v_mov_b32_e32 v142, v145
	v_cvt_pk_bf16_f32 v157, v154, v155
	v_pk_add_f32 v[136:137], v[136:137], v[138:139]
	v_pk_add_f32 v[132:133], v[194:195], v[204:205]
	global_store_dwordx2 v[240:241], v[156:157], off offset:2560
	v_pk_mul_f32 v[152:153], v[152:153], v[2:3] op_sel_hi:[1,0]
	v_pk_mul_f32 v[148:149], v[148:149], v[2:3] op_sel_hi:[1,0]
	v_pk_mul_f32 v[142:143], v[142:143], v[2:3] op_sel_hi:[1,0]
	v_pk_mul_f32 v[144:145], v[146:147], v[2:3] op_sel_hi:[1,0]
	v_add_f32_e32 v2, 0, v136
	s_waitcnt vmcnt(26)
	v_lshlrev_b32_e32 v188, 16, v128
	v_and_b32_e32 v189, 0xffff0000, v128
	v_lshlrev_b32_e32 v190, 16, v129
	v_and_b32_e32 v191, 0xffff0000, v129
	s_waitcnt vmcnt(25)
	v_lshlrev_b32_e32 v213, 16, v124
	v_and_b32_e32 v183, 0xffff0000, v124
	v_lshlrev_b32_e32 v157, 16, v125
	v_and_b32_e32 v155, 0xffff0000, v125
	v_pk_add_f32 v[124:125], v[132:133], v[132:133] op_sel:[0,1] op_sel_hi:[1,0]
	v_add_f32_e32 v212, v2, v137
	v_add_f32_e32 v156, v188, v189
	v_add_f32_e32 v154, v190, v191
	v_mov_b32_e32 v125, v183
	v_pk_add_f32 v[124:125], v[212:213], v[124:125]
	v_pk_add_f32 v[128:129], v[156:157], v[154:155]
	s_waitcnt vmcnt(24)
	v_lshlrev_b32_e32 v185, 16, v121
	v_lshlrev_b32_e32 v184, 16, v120
	v_and_b32_e32 v187, 0xffff0000, v121
	v_and_b32_e32 v186, 0xffff0000, v120
	v_pk_fma_f32 v[152:153], v[56:57], v[152:153], v[60:61]
	v_pk_fma_f32 v[148:149], v[54:55], v[148:149], v[58:59]
	v_pk_add_f32 v[124:125], v[124:125], v[128:129]
	v_pk_add_f32 v[120:121], v[184:185], v[186:187]
	v_cvt_pk_bf16_f32 v148, v148, v149
	v_cvt_pk_bf16_f32 v149, v152, v153
	s_waitcnt vmcnt(23)
	v_lshlrev_b32_e32 v138, 16, v116
	v_and_b32_e32 v139, 0xffff0000, v116
	v_lshlrev_b32_e32 v152, 16, v117
	v_and_b32_e32 v153, 0xffff0000, v117
	s_waitcnt vmcnt(22)
	v_lshlrev_b32_e32 v136, 16, v112
	v_and_b32_e32 v137, 0xffff0000, v112
	v_lshlrev_b32_e32 v133, 16, v113
	v_and_b32_e32 v129, 0xffff0000, v113
	v_pk_add_f32 v[112:113], v[124:125], v[124:125] op_sel:[0,1] op_sel_hi:[1,0]
	v_pk_add_f32 v[116:117], v[120:121], v[120:121] op_sel:[0,1] op_sel_hi:[1,0]
	v_add_f32_e32 v132, v138, v139
	v_add_f32_e32 v128, v152, v153
	v_mov_b32_e32 v113, v136
	v_mov_b32_e32 v117, v137
	v_pk_add_f32 v[112:113], v[112:113], v[116:117]
	v_pk_add_f32 v[116:117], v[132:133], v[128:129]
	s_movk_i32 s8, 0x5000
	v_pk_add_f32 v[112:113], v[112:113], v[116:117]
	v_pk_fma_f32 v[144:145], v[46:47], v[144:145], v[50:51]
	v_add_f32_e32 v2, v112, v113
	v_add_co_u32_e32 v112, vcc, s8, v110
	global_store_dwordx2 v[240:241], v[148:149], off offset:3072
	v_pk_fma_f32 v[142:143], v[48:49], v[142:143], v[52:53]
	s_waitcnt lgkmcnt(0)
	s_nop 1
	v_add_f32_dpp v2, v2, v2 quad_perm:[1,0,3,2] row_mask:0xf bank_mask:0xf
	v_cvt_pk_bf16_f32 v144, v144, v145
	v_cvt_pk_bf16_f32 v145, v142, v143
	global_store_dwordx2 v[240:241], v[144:145], off offset:3584
	v_addc_co_u32_e32 v113, vcc, 0, v111, vcc
	s_waitcnt lgkmcnt(0)
	s_nop 1
	v_add_f32_dpp v2, v2, v2 quad_perm:[2,3,0,1] row_mask:0xf bank_mask:0xf
	global_load_dwordx2 v[146:147], v[112:113], off
	global_load_dwordx2 v[148:149], v[112:113], off offset:512
	global_load_dwordx2 v[144:145], v[112:113], off offset:1024
	global_load_dwordx2 v[142:143], v[112:113], off offset:1536
	global_load_dwordx2 v[124:125], v[112:113], off offset:2048
	global_load_dwordx2 v[120:121], v[112:113], off offset:2560
	global_load_dwordx2 v[116:117], v[112:113], off offset:3072
	s_nop 0
	global_load_dwordx2 v[112:113], v[112:113], off offset:3584
	s_waitcnt lgkmcnt(0)
	s_nop 1
	v_add_f32_dpp v2, v2, v2 row_half_mirror row_mask:0xf bank_mask:0xf
	s_waitcnt lgkmcnt(0)
	s_nop 1
	v_add_f32_dpp v2, v2, v2 row_mirror row_mask:0xf bank_mask:0xf
	s_waitcnt lgkmcnt(0)
	v_mov_b32_e32 v128, v2
	s_nop 1
	v_permlane16_swap_b32_e32 v128, v2
	v_add_f32_e32 v2, v2, v128
	s_waitcnt lgkmcnt(0)
	v_mov_b32_e32 v128, v2
	s_nop 1
	v_permlane32_swap_b32_e32 v128, v2
	v_add_f32_e32 v128, v2, v128
	v_fmac_f32_e32 v208, 0xba000000, v128
	v_fmac_f32_e32 v192, 0xba000000, v128
	v_fmac_f32_e32 v206, 0xba000000, v128
	v_fmac_f32_e32 v210, 0xba000000, v128
	v_mul_f32_e32 v2, v192, v192
	v_mul_f32_e32 v132, v208, v208
	v_fmac_f32_e32 v2, v210, v210
	v_fmac_f32_e32 v132, v206, v206
	v_fmac_f32_e32 v209, 0xba000000, v128
	v_fmac_f32_e32 v193, 0xba000000, v128
	v_add_f32_e32 v2, v2, v132
	v_fmac_f32_e32 v207, 0xba000000, v128
	v_fmac_f32_e32 v211, 0xba000000, v128
	v_mul_f32_e32 v132, v193, v193
	v_mul_f32_e32 v154, v209, v209
	v_fmac_f32_e32 v132, v211, v211
	v_fmac_f32_e32 v154, v207, v207
	v_add_f32_e32 v132, v132, v154
	v_fmac_f32_e32 v205, 0xba000000, v128
	v_fmac_f32_e32 v204, 0xba000000, v128
	v_add_f32_e32 v2, v2, v132
	v_fmac_f32_e32 v195, 0xba000000, v128
	v_fmac_f32_e32 v194, 0xba000000, v128
	v_mul_f32_e32 v132, v204, v204
	v_mul_f32_e32 v154, v205, v205
	v_fmac_f32_e32 v132, v194, v194
	v_fmac_f32_e32 v154, v195, v195
	v_add_f32_e32 v132, v132, v154
	v_fmac_f32_e32 v191, 0xba000000, v128
	v_fmac_f32_e32 v189, 0xba000000, v128
	v_add_f32_e32 v2, v132, v2
	v_fmac_f32_e32 v190, 0xba000000, v128
	v_fmac_f32_e32 v188, 0xba000000, v128
	v_mul_f32_e32 v132, v189, v189
	v_mul_f32_e32 v154, v191, v191
	v_fmac_f32_e32 v132, v188, v188
	v_fmac_f32_e32 v154, v190, v190
	v_add_f32_e32 v132, v132, v154
	v_fmac_f32_e32 v155, 0xba000000, v128
	v_fmac_f32_e32 v183, 0xba000000, v128
	v_add_f32_e32 v2, v132, v2
	v_fmac_f32_e32 v157, 0xba000000, v128
	v_fmac_f32_e32 v213, 0xba000000, v128
	v_mul_f32_e32 v132, v183, v183
	v_mul_f32_e32 v154, v155, v155
	v_fmac_f32_e32 v132, v213, v213
	v_fmac_f32_e32 v154, v157, v157
	v_add_f32_e32 v132, v132, v154
	v_fmac_f32_e32 v187, 0xba000000, v128
	v_fmac_f32_e32 v186, 0xba000000, v128
	v_add_f32_e32 v2, v132, v2
	v_fmac_f32_e32 v185, 0xba000000, v128
	v_fmac_f32_e32 v184, 0xba000000, v128
	v_mul_f32_e32 v132, v186, v186
	v_mul_f32_e32 v154, v187, v187
	v_fmac_f32_e32 v132, v184, v184
	v_fmac_f32_e32 v154, v185, v185
	v_add_f32_e32 v132, v132, v154
	v_fmac_f32_e32 v153, 0xba000000, v128
	v_fmac_f32_e32 v139, 0xba000000, v128
	v_add_f32_e32 v2, v132, v2
	v_fmac_f32_e32 v152, 0xba000000, v128
	v_fmac_f32_e32 v138, 0xba000000, v128
	v_mul_f32_e32 v132, v139, v139
	v_mul_f32_e32 v154, v153, v153
	v_fmac_f32_e32 v132, v138, v138
	v_fmac_f32_e32 v154, v152, v152
	v_add_f32_e32 v132, v132, v154
	v_fmac_f32_e32 v129, 0xba000000, v128
	v_fmac_f32_e32 v137, 0xba000000, v128
	v_add_f32_e32 v2, v132, v2
	v_fmac_f32_e32 v133, 0xba000000, v128
	v_fmac_f32_e32 v136, 0xba000000, v128
	v_mul_f32_e32 v132, v137, v137
	v_mul_f32_e32 v154, v129, v129
	v_fmac_f32_e32 v132, v136, v136
	v_fmac_f32_e32 v154, v133, v133
	v_add_f32_e32 v132, v132, v154
	v_add_f32_e32 v2, v132, v2
	s_waitcnt lgkmcnt(0)
	s_nop 1
	v_add_f32_dpp v2, v2, v2 quad_perm:[1,0,3,2] row_mask:0xf bank_mask:0xf
	s_waitcnt lgkmcnt(0)
	s_nop 1
	v_add_f32_dpp v2, v2, v2 quad_perm:[2,3,0,1] row_mask:0xf bank_mask:0xf
	s_waitcnt lgkmcnt(0)
	s_nop 1
	v_add_f32_dpp v2, v2, v2 row_half_mirror row_mask:0xf bank_mask:0xf
	s_waitcnt lgkmcnt(0)
	s_nop 1
	v_add_f32_dpp v2, v2, v2 row_mirror row_mask:0xf bank_mask:0xf
	s_waitcnt lgkmcnt(0)
	v_mov_b32_e32 v132, v2
	s_nop 1
	v_permlane16_swap_b32_e32 v132, v2
	v_add_f32_e32 v2, v2, v132
	s_waitcnt lgkmcnt(0)
	v_mov_b32_e32 v132, v2
	s_nop 1
	v_permlane32_swap_b32_e32 v132, v2
	v_add_f32_e32 v2, v2, v132
	v_fmamk_f32 v2, v2, 0x3a000000, v217
	v_cmp_gt_f32_e32 vcc, s87, v2
	v_mul_f32_e32 v132, 0x4f800000, v2
	s_nop 0
	v_cndmask_b32_e32 v2, v2, v132, vcc
	v_sqrt_f32_e32 v132, v2
	s_nop 0
	v_add_u32_e32 v154, -1, v132
	v_fma_f32 v156, -v154, v132, v2
	v_cmp_ge_f32_e64 s[8:9], 0, v156
	v_add_u32_e32 v156, 1, v132
	s_nop 0
	v_cndmask_b32_e64 v154, v132, v154, s[8:9]
	v_fma_f32 v132, -v156, v132, v2
	v_cmp_lt_f32_e64 s[8:9], 0, v132
	s_nop 1
	v_cndmask_b32_e64 v132, v154, v156, s[8:9]
	v_mul_f32_e32 v154, 0x37800000, v132
	v_cndmask_b32_e32 v132, v132, v154, vcc
	v_cmp_class_f32_e32 vcc, v2, v218
	s_nop 1
	v_cndmask_b32_e32 v2, v132, v2, vcc
	v_div_scale_f32 v132, s[8:9], v2, v2, 1.0
	v_rcp_f32_e32 v154, v132
	s_nop 0
	v_fma_f32 v156, -v132, v154, 1.0
	v_fmac_f32_e32 v154, v156, v154
	v_div_scale_f32 v156, vcc, 1.0, v2, 1.0
	v_mul_f32_e32 v182, v156, v154
	v_fma_f32 v212, -v132, v182, v156
	v_fmac_f32_e32 v182, v212, v154
	v_fma_f32 v132, -v132, v182, v156
	v_div_fmas_f32 v132, v132, v154, v182
	v_div_fixup_f32 v2, v132, v2, 1.0
	s_and_saveexec_b64 s[8:9], s[4:5]
	s_add_i32 s10, s78, 0
	v_mul_f32_e32 v214, 0x3a000000, v128
	v_mov_b32_e32 v215, v2
	v_mov_b32_e32 v128, s10
	ds_write_b64 v128, v[214:215] offset:33816
	s_or_b64 exec, exec, s[8:9]
	v_mov_b32_e32 v214, v210
	v_mov_b32_e32 v215, v192
	v_mov_b32_e32 v240, v206
	v_mov_b32_e32 v241, v208
	v_pk_mul_f32 v[240:241], v[240:241], v[2:3] op_sel_hi:[1,0]
	v_pk_mul_f32 v[214:215], v[214:215], v[2:3] op_sel_hi:[1,0]
	v_mov_b32_e32 v192, v211
	v_pk_fma_f32 v[240:241], v[104:105], v[240:241], v[108:109]
	v_pk_fma_f32 v[214:215], v[102:103], v[214:215], v[106:107]
	s_movk_i32 s8, 0x3000
	v_cvt_pk_bf16_f32 v214, v214, v215
	v_cvt_pk_bf16_f32 v215, v240, v241
	v_add_co_u32_e32 v240, vcc, s8, v4
	v_mov_b32_e32 v208, v207
	v_pk_mul_f32 v[192:193], v[192:193], v[2:3] op_sel_hi:[1,0]
	v_mov_b32_e32 v210, v194
	v_mov_b32_e32 v211, v204
	v_mov_b32_e32 v182, v213
	v_addc_co_u32_e32 v241, vcc, 0, v5, vcc
	v_pk_mul_f32 v[206:207], v[208:209], v[2:3] op_sel_hi:[1,0]
	v_pk_fma_f32 v[192:193], v[94:95], v[192:193], v[98:99]
	global_store_dwordx2 v[240:241], v[214:215], off
	v_pk_fma_f32 v[206:207], v[96:97], v[206:207], v[100:101]
	v_cvt_pk_bf16_f32 v192, v192, v193
	v_mov_b32_e32 v204, v195
	v_cvt_pk_bf16_f32 v193, v206, v207
	v_pk_mul_f32 v[194:195], v[210:211], v[2:3] op_sel_hi:[1,0]
	v_pk_mul_f32 v[188:189], v[188:189], v[2:3] op_sel_hi:[1,0]
	v_mov_b32_e32 v154, v157
	v_pk_mul_f32 v[156:157], v[182:183], v[2:3] op_sel_hi:[1,0]
	global_store_dwordx2 v[240:241], v[192:193], off offset:512
	v_pk_mul_f32 v[192:193], v[204:205], v[2:3] op_sel_hi:[1,0]
	v_pk_fma_f32 v[194:195], v[86:87], v[194:195], v[90:91]
	v_pk_mul_f32 v[190:191], v[190:191], v[2:3] op_sel_hi:[1,0]
	v_pk_fma_f32 v[188:189], v[78:79], v[188:189], v[82:83]
	v_pk_mul_f32 v[154:155], v[154:155], v[2:3] op_sel_hi:[1,0]
	v_pk_fma_f32 v[156:157], v[70:71], v[156:157], v[74:75]
	v_mov_b32_e32 v212, v184
	v_mov_b32_e32 v213, v186
	v_pk_fma_f32 v[192:193], v[88:89], v[192:193], v[92:93]
	v_cvt_pk_bf16_f32 v194, v194, v195
	v_pk_fma_f32 v[190:191], v[80:81], v[190:191], v[84:85]
	v_cvt_pk_bf16_f32 v195, v192, v193
	global_store_dwordx2 v[240:241], v[194:195], off offset:1024
	v_cvt_pk_bf16_f32 v188, v188, v189
	v_cvt_pk_bf16_f32 v189, v190, v191
	global_store_dwordx2 v[240:241], v[188:189], off offset:1536
	v_pk_fma_f32 v[154:155], v[72:73], v[154:155], v[76:77]
	v_cvt_pk_bf16_f32 v156, v156, v157
	v_mov_b32_e32 v186, v185
	v_cvt_pk_bf16_f32 v157, v154, v155
	global_store_dwordx2 v[240:241], v[156:157], off offset:2048
	v_pk_mul_f32 v[156:157], v[212:213], v[2:3] op_sel_hi:[1,0]
	v_pk_mul_f32 v[138:139], v[138:139], v[2:3] op_sel_hi:[1,0]
	v_mov_b32_e32 v128, v133
	v_pk_mul_f32 v[132:133], v[136:137], v[2:3] op_sel_hi:[1,0]
	v_pk_mul_f32 v[154:155], v[186:187], v[2:3] op_sel_hi:[1,0]
	v_pk_fma_f32 v[156:157], v[62:63], v[156:157], v[66:67]
	v_pk_mul_f32 v[152:153], v[152:153], v[2:3] op_sel_hi:[1,0]
	v_pk_fma_f32 v[138:139], v[54:55], v[138:139], v[58:59]
	v_pk_mul_f32 v[128:129], v[128:129], v[2:3] op_sel_hi:[1,0]
	v_pk_fma_f32 v[132:133], v[46:47], v[132:133], v[50:51]
	v_pk_fma_f32 v[154:155], v[64:65], v[154:155], v[68:69]
	v_cvt_pk_bf16_f32 v156, v156, v157
	v_pk_fma_f32 v[152:153], v[56:57], v[152:153], v[60:61]
	v_cvt_pk_bf16_f32 v157, v154, v155
	global_store_dwordx2 v[240:241], v[156:157], off offset:2560
	v_cvt_pk_bf16_f32 v138, v138, v139
	v_cvt_pk_bf16_f32 v139, v152, v153
	global_store_dwordx2 v[240:241], v[138:139], off offset:3072
	v_pk_fma_f32 v[128:129], v[48:49], v[128:129], v[52:53]
	v_cvt_pk_bf16_f32 v132, v132, v133
	s_waitcnt vmcnt(29)
	v_lshlrev_b32_e32 v213, 16, v150
	v_cvt_pk_bf16_f32 v133, v128, v129
	v_lshlrev_b32_e32 v212, 16, v140
	v_and_b32_e32 v195, 0xffff0000, v150
	v_and_b32_e32 v194, 0xffff0000, v140
	v_lshlrev_b32_e32 v209, 16, v151
	v_lshlrev_b32_e32 v208, 16, v141
	v_and_b32_e32 v211, 0xffff0000, v151
	v_and_b32_e32 v210, 0xffff0000, v141
	global_store_dwordx2 v[240:241], v[132:133], off offset:3584
	v_pk_add_f32 v[128:129], v[212:213], v[194:195]
	v_pk_add_f32 v[132:133], v[208:209], v[210:211]
	s_waitcnt vmcnt(29)
	v_lshlrev_b32_e32 v205, 16, v135
	v_pk_add_f32 v[128:129], v[128:129], v[132:133]
	v_lshlrev_b32_e32 v204, 16, v134
	v_add_f32_e32 v2, 0, v128
	v_and_b32_e32 v207, 0xffff0000, v135
	v_and_b32_e32 v206, 0xffff0000, v134
	v_add_f32_e32 v214, v2, v129
	v_pk_add_f32 v[128:129], v[204:205], v[206:207]
	s_waitcnt vmcnt(28)
	v_lshlrev_b32_e32 v190, 16, v130
	v_and_b32_e32 v191, 0xffff0000, v130
	v_lshlrev_b32_e32 v192, 16, v131
	v_and_b32_e32 v193, 0xffff0000, v131
	s_waitcnt vmcnt(27)
	v_lshlrev_b32_e32 v215, 16, v126
	v_and_b32_e32 v187, 0xffff0000, v126
	v_lshlrev_b32_e32 v185, 16, v127
	v_and_b32_e32 v157, 0xffff0000, v127
	v_pk_add_f32 v[126:127], v[128:129], v[128:129] op_sel:[0,1] op_sel_hi:[1,0]
	v_add_f32_e32 v184, v190, v191
	v_add_f32_e32 v156, v192, v193
	v_mov_b32_e32 v127, v187
	v_pk_add_f32 v[126:127], v[214:215], v[126:127]
	v_pk_add_f32 v[128:129], v[184:185], v[156:157]
	s_waitcnt vmcnt(26)
	v_lshlrev_b32_e32 v183, 16, v123
	v_lshlrev_b32_e32 v182, 16, v122
	v_and_b32_e32 v189, 0xffff0000, v123
	v_and_b32_e32 v188, 0xffff0000, v122
	v_pk_add_f32 v[126:127], v[126:127], v[128:129]
	v_pk_add_f32 v[128:129], v[182:183], v[188:189]
	s_waitcnt vmcnt(25)
	v_lshlrev_b32_e32 v152, 16, v118
	v_and_b32_e32 v153, 0xffff0000, v118
	v_lshlrev_b32_e32 v154, 16, v119
	v_and_b32_e32 v155, 0xffff0000, v119
	s_waitcnt vmcnt(24)
	v_lshlrev_b32_e32 v150, 16, v114
	v_and_b32_e32 v151, 0xffff0000, v114
	v_lshlrev_b32_e32 v123, 16, v115
	v_and_b32_e32 v119, 0xffff0000, v115
	v_pk_add_f32 v[114:115], v[126:127], v[126:127] op_sel:[0,1] op_sel_hi:[1,0]
	v_pk_add_f32 v[126:127], v[128:129], v[128:129] op_sel:[0,1] op_sel_hi:[1,0]
	v_add_f32_e32 v122, v152, v153
	v_add_f32_e32 v118, v154, v155
	v_mov_b32_e32 v115, v150
	v_mov_b32_e32 v127, v151
	v_pk_add_f32 v[114:115], v[114:115], v[126:127]
	v_pk_add_f32 v[126:127], v[122:123], v[118:119]
	s_movk_i32 s8, 0x6000
	v_pk_add_f32 v[114:115], v[114:115], v[126:127]
	s_nop 0
	v_add_f32_e32 v2, v114, v115
	v_add_co_u32_e32 v114, vcc, s8, v110
	s_nop 1
	v_addc_co_u32_e32 v115, vcc, 0, v111, vcc
	global_load_dwordx2 v[138:139], v[114:115], off
	global_load_dwordx2 v[140:141], v[114:115], off offset:512
	global_load_dwordx2 v[136:137], v[114:115], off offset:1024
	global_load_dwordx2 v[134:135], v[114:115], off offset:1536
	global_load_dwordx2 v[132:133], v[114:115], off offset:2048
	global_load_dwordx2 v[130:131], v[114:115], off offset:2560
	global_load_dwordx2 v[128:129], v[114:115], off offset:3072
	global_load_dwordx2 v[126:127], v[114:115], off offset:3584
	s_waitcnt lgkmcnt(0)
	s_nop 1
	v_add_f32_dpp v2, v2, v2 quad_perm:[1,0,3,2] row_mask:0xf bank_mask:0xf
	s_waitcnt lgkmcnt(0)
	s_nop 1
	v_add_f32_dpp v2, v2, v2 quad_perm:[2,3,0,1] row_mask:0xf bank_mask:0xf
	s_waitcnt lgkmcnt(0)
	s_nop 1
	v_add_f32_dpp v2, v2, v2 row_half_mirror row_mask:0xf bank_mask:0xf
	s_waitcnt lgkmcnt(0)
	s_nop 1
	v_add_f32_dpp v2, v2, v2 row_mirror row_mask:0xf bank_mask:0xf
	s_waitcnt lgkmcnt(0)
	v_mov_b32_e32 v114, v2
	s_nop 1
	v_permlane16_swap_b32_e32 v114, v2
	v_add_f32_e32 v2, v2, v114
	s_waitcnt lgkmcnt(0)
	v_mov_b32_e32 v114, v2
	s_nop 1
	v_permlane32_swap_b32_e32 v114, v2
	v_add_f32_e32 v114, v2, v114
	v_fmac_f32_e32 v210, 0xba000000, v114
	v_fmac_f32_e32 v194, 0xba000000, v114
	v_fmac_f32_e32 v208, 0xba000000, v114
	v_fmac_f32_e32 v212, 0xba000000, v114
	v_mul_f32_e32 v2, v194, v194
	v_mul_f32_e32 v115, v210, v210
	v_fmac_f32_e32 v2, v212, v212
	v_fmac_f32_e32 v115, v208, v208
	v_fmac_f32_e32 v211, 0xba000000, v114
	v_fmac_f32_e32 v195, 0xba000000, v114
	v_add_f32_e32 v2, v2, v115
	v_fmac_f32_e32 v209, 0xba000000, v114
	v_fmac_f32_e32 v213, 0xba000000, v114
	v_mul_f32_e32 v115, v195, v195
	v_mul_f32_e32 v118, v211, v211
	v_fmac_f32_e32 v115, v213, v213
	v_fmac_f32_e32 v118, v209, v209
	v_add_f32_e32 v115, v115, v118
	v_fmac_f32_e32 v207, 0xba000000, v114
	v_fmac_f32_e32 v206, 0xba000000, v114
	v_add_f32_e32 v2, v2, v115
	v_fmac_f32_e32 v205, 0xba000000, v114
	v_fmac_f32_e32 v204, 0xba000000, v114
	v_mul_f32_e32 v115, v206, v206
	v_mul_f32_e32 v118, v207, v207
	v_fmac_f32_e32 v115, v204, v204
	v_fmac_f32_e32 v118, v205, v205
	v_add_f32_e32 v115, v115, v118
	v_fmac_f32_e32 v193, 0xba000000, v114
	v_fmac_f32_e32 v191, 0xba000000, v114
	v_add_f32_e32 v2, v115, v2
	v_fmac_f32_e32 v192, 0xba000000, v114
	v_fmac_f32_e32 v190, 0xba000000, v114
	v_mul_f32_e32 v115, v191, v191
	v_mul_f32_e32 v118, v193, v193
	v_fmac_f32_e32 v115, v190, v190
	v_fmac_f32_e32 v118, v192, v192
	v_add_f32_e32 v115, v115, v118
	v_fmac_f32_e32 v157, 0xba000000, v114
	v_fmac_f32_e32 v187, 0xba000000, v114
	v_add_f32_e32 v2, v115, v2
	v_fmac_f32_e32 v185, 0xba000000, v114
	v_fmac_f32_e32 v215, 0xba000000, v114
	v_mul_f32_e32 v115, v187, v187
	v_mul_f32_e32 v118, v157, v157
	v_fmac_f32_e32 v115, v215, v215
	v_fmac_f32_e32 v118, v185, v185
	v_add_f32_e32 v115, v115, v118
	v_fmac_f32_e32 v189, 0xba000000, v114
	v_fmac_f32_e32 v188, 0xba000000, v114
	v_add_f32_e32 v2, v115, v2
	v_fmac_f32_e32 v183, 0xba000000, v114
	v_fmac_f32_e32 v182, 0xba000000, v114
	v_mul_f32_e32 v115, v188, v188
	v_mul_f32_e32 v118, v189, v189
	v_fmac_f32_e32 v115, v182, v182
	v_fmac_f32_e32 v118, v183, v183
	v_add_f32_e32 v115, v115, v118
	v_fmac_f32_e32 v155, 0xba000000, v114
	v_fmac_f32_e32 v153, 0xba000000, v114
	v_add_f32_e32 v2, v115, v2
	v_fmac_f32_e32 v154, 0xba000000, v114
	v_fmac_f32_e32 v152, 0xba000000, v114
	v_mul_f32_e32 v115, v153, v153
	v_mul_f32_e32 v118, v155, v155
	v_fmac_f32_e32 v115, v152, v152
	v_fmac_f32_e32 v118, v154, v154
	v_add_f32_e32 v115, v115, v118
	v_fmac_f32_e32 v119, 0xba000000, v114
	v_fmac_f32_e32 v151, 0xba000000, v114
	v_add_f32_e32 v2, v115, v2
	v_fmac_f32_e32 v123, 0xba000000, v114
	v_fmac_f32_e32 v150, 0xba000000, v114
	v_mul_f32_e32 v115, v151, v151
	v_mul_f32_e32 v118, v119, v119
	v_fmac_f32_e32 v115, v150, v150
	v_fmac_f32_e32 v118, v123, v123
	v_add_f32_e32 v115, v115, v118
	v_add_f32_e32 v2, v115, v2
	s_waitcnt lgkmcnt(0)
	s_nop 1
	v_add_f32_dpp v2, v2, v2 quad_perm:[1,0,3,2] row_mask:0xf bank_mask:0xf
	s_waitcnt lgkmcnt(0)
	s_nop 1
	v_add_f32_dpp v2, v2, v2 quad_perm:[2,3,0,1] row_mask:0xf bank_mask:0xf
	s_waitcnt lgkmcnt(0)
	s_nop 1
	v_add_f32_dpp v2, v2, v2 row_half_mirror row_mask:0xf bank_mask:0xf
	s_waitcnt lgkmcnt(0)
	s_nop 1
	v_add_f32_dpp v2, v2, v2 row_mirror row_mask:0xf bank_mask:0xf
	s_waitcnt lgkmcnt(0)
	v_mov_b32_e32 v115, v2
	s_nop 1
	v_permlane16_swap_b32_e32 v115, v2
	v_add_f32_e32 v2, v2, v115
	s_waitcnt lgkmcnt(0)
	v_mov_b32_e32 v115, v2
	s_nop 1
	v_permlane32_swap_b32_e32 v115, v2
	v_add_f32_e32 v2, v2, v115
	v_fmamk_f32 v2, v2, 0x3a000000, v217
	v_cmp_gt_f32_e32 vcc, s87, v2
	v_mul_f32_e32 v115, 0x4f800000, v2
	s_nop 0
	v_cndmask_b32_e32 v2, v2, v115, vcc
	v_sqrt_f32_e32 v115, v2
	s_nop 0
	v_add_u32_e32 v118, -1, v115
	v_fma_f32 v122, -v118, v115, v2
	v_cmp_ge_f32_e64 s[8:9], 0, v122
	v_add_u32_e32 v122, 1, v115
	s_nop 0
	v_cndmask_b32_e64 v118, v115, v118, s[8:9]
	v_fma_f32 v115, -v122, v115, v2
	v_cmp_lt_f32_e64 s[8:9], 0, v115
	s_nop 1
	v_cndmask_b32_e64 v115, v118, v122, s[8:9]
	v_mul_f32_e32 v118, 0x37800000, v115
	v_cndmask_b32_e32 v115, v115, v118, vcc
	v_cmp_class_f32_e32 vcc, v2, v218
	s_nop 1
	v_cndmask_b32_e32 v2, v115, v2, vcc
	v_div_scale_f32 v115, s[8:9], v2, v2, 1.0
	v_rcp_f32_e32 v118, v115
	s_nop 0
	v_fma_f32 v122, -v115, v118, 1.0
	v_fmac_f32_e32 v118, v122, v118
	v_div_scale_f32 v122, vcc, 1.0, v2, 1.0
	v_mul_f32_e32 v156, v122, v118
	v_fma_f32 v184, -v115, v156, v122
	v_fmac_f32_e32 v156, v184, v118
	v_fma_f32 v115, -v115, v156, v122
	v_div_fmas_f32 v115, v115, v118, v156
	v_div_fixup_f32 v2, v115, v2, 1.0
	s_and_saveexec_b64 s[8:9], s[4:5]
	s_add_i32 s10, s78, 0
	v_mul_f32_e32 v114, 0x3a000000, v114
	v_mov_b32_e32 v115, v2
	v_mov_b32_e32 v118, s10
	ds_write_b64 v118, v[114:115] offset:33824
	s_or_b64 exec, exec, s[8:9]
	v_mov_b32_e32 v114, v212
	v_mov_b32_e32 v115, v194
	v_mov_b32_e32 v240, v208
	v_mov_b32_e32 v241, v210
	v_pk_mul_f32 v[240:241], v[240:241], v[2:3] op_sel_hi:[1,0]
	v_pk_mul_f32 v[114:115], v[114:115], v[2:3] op_sel_hi:[1,0]
	v_pk_fma_f32 v[240:241], v[104:105], v[240:241], v[108:109]
	v_pk_fma_f32 v[114:115], v[102:103], v[114:115], v[106:107]
	s_movk_i32 s8, 0x4000
	v_mov_b32_e32 v194, v213
	v_cvt_pk_bf16_f32 v114, v114, v115
	v_cvt_pk_bf16_f32 v115, v240, v241
	v_add_co_u32_e32 v240, vcc, s8, v4
	v_mov_b32_e32 v210, v209
	s_nop 0
	v_addc_co_u32_e32 v241, vcc, 0, v5, vcc
	v_pk_mul_f32 v[194:195], v[194:195], v[2:3] op_sel_hi:[1,0]
	global_store_dwordx2 v[240:241], v[114:115], off
	v_pk_mul_f32 v[114:115], v[210:211], v[2:3] op_sel_hi:[1,0]
	v_pk_fma_f32 v[194:195], v[94:95], v[194:195], v[98:99]
	v_mov_b32_e32 v212, v204
	v_mov_b32_e32 v213, v206
	v_pk_fma_f32 v[114:115], v[96:97], v[114:115], v[100:101]
	v_cvt_pk_bf16_f32 v194, v194, v195
	v_mov_b32_e32 v206, v205
	v_cvt_pk_bf16_f32 v195, v114, v115
	global_store_dwordx2 v[240:241], v[194:195], off offset:512
	v_pk_mul_f32 v[114:115], v[206:207], v[2:3] op_sel_hi:[1,0]
	v_pk_mul_f32 v[194:195], v[212:213], v[2:3] op_sel_hi:[1,0]
	v_pk_fma_f32 v[114:115], v[88:89], v[114:115], v[92:93]
	v_pk_fma_f32 v[194:195], v[86:87], v[194:195], v[90:91]
	v_pk_mul_f32 v[190:191], v[190:191], v[2:3] op_sel_hi:[1,0]
	v_cvt_pk_bf16_f32 v194, v194, v195
	v_cvt_pk_bf16_f32 v195, v114, v115
	v_pk_mul_f32 v[114:115], v[192:193], v[2:3] op_sel_hi:[1,0]
	v_mov_b32_e32 v186, v215
	v_pk_fma_f32 v[114:115], v[80:81], v[114:115], v[84:85]
	v_pk_fma_f32 v[190:191], v[78:79], v[190:191], v[82:83]
	v_mov_b32_e32 v156, v185
	global_store_dwordx2 v[240:241], v[194:195], off offset:1024
	v_cvt_pk_bf16_f32 v190, v190, v191
	v_cvt_pk_bf16_f32 v191, v114, v115
	v_pk_mul_f32 v[114:115], v[156:157], v[2:3] op_sel_hi:[1,0]
	v_pk_mul_f32 v[156:157], v[186:187], v[2:3] op_sel_hi:[1,0]
	v_mov_b32_e32 v214, v182
	v_pk_fma_f32 v[156:157], v[70:71], v[156:157], v[74:75]
	v_mov_b32_e32 v215, v188
	global_store_dwordx2 v[240:241], v[190:191], off offset:1536
	v_pk_fma_f32 v[114:115], v[72:73], v[114:115], v[76:77]
	v_cvt_pk_bf16_f32 v156, v156, v157
	v_mov_b32_e32 v188, v183
	v_cvt_pk_bf16_f32 v157, v114, v115
	global_store_dwordx2 v[240:241], v[156:157], off offset:2048
	v_pk_mul_f32 v[114:115], v[188:189], v[2:3] op_sel_hi:[1,0]
	v_pk_mul_f32 v[156:157], v[214:215], v[2:3] op_sel_hi:[1,0]
	v_pk_fma_f32 v[114:115], v[64:65], v[114:115], v[68:69]
	v_pk_fma_f32 v[156:157], v[62:63], v[156:157], v[66:67]
	v_pk_mul_f32 v[152:153], v[152:153], v[2:3] op_sel_hi:[1,0]
	v_cvt_pk_bf16_f32 v156, v156, v157
	v_cvt_pk_bf16_f32 v157, v114, v115
	v_pk_mul_f32 v[114:115], v[154:155], v[2:3] op_sel_hi:[1,0]
	v_pk_fma_f32 v[152:153], v[54:55], v[152:153], v[58:59]
	v_pk_fma_f32 v[114:115], v[56:57], v[114:115], v[60:61]
	v_mov_b32_e32 v118, v123
	global_store_dwordx2 v[240:241], v[156:157], off offset:2560
	v_cvt_pk_bf16_f32 v152, v152, v153
	v_cvt_pk_bf16_f32 v153, v114, v115
	v_pk_mul_f32 v[114:115], v[118:119], v[2:3] op_sel_hi:[1,0]
	v_pk_mul_f32 v[118:119], v[150:151], v[2:3] op_sel_hi:[1,0]
	global_store_dwordx2 v[240:241], v[152:153], off offset:3072
	v_pk_fma_f32 v[118:119], v[46:47], v[118:119], v[50:51]
	v_pk_fma_f32 v[114:115], v[48:49], v[114:115], v[52:53]
	v_cvt_pk_bf16_f32 v118, v118, v119
	s_waitcnt vmcnt(29)
	v_lshlrev_b32_e32 v209, 16, v148
	v_cvt_pk_bf16_f32 v119, v114, v115
	v_lshlrev_b32_e32 v208, 16, v146
	v_and_b32_e32 v151, 0xffff0000, v148
	v_and_b32_e32 v150, 0xffff0000, v146
	v_lshlrev_b32_e32 v153, 16, v149
	v_lshlrev_b32_e32 v152, 16, v147
	v_and_b32_e32 v149, 0xffff0000, v149
	v_and_b32_e32 v148, 0xffff0000, v147
	global_store_dwordx2 v[240:241], v[118:119], off offset:3584
	v_pk_add_f32 v[114:115], v[208:209], v[150:151]
	v_pk_add_f32 v[118:119], v[152:153], v[148:149]
	s_waitcnt vmcnt(29)
	v_lshlrev_b32_e32 v155, 16, v145
	v_pk_add_f32 v[114:115], v[114:115], v[118:119]
	v_lshlrev_b32_e32 v154, 16, v144
	v_add_f32_e32 v2, 0, v114
	v_and_b32_e32 v185, 0xffff0000, v145
	v_and_b32_e32 v184, 0xffff0000, v144
	v_add_f32_e32 v210, v2, v115
	v_pk_add_f32 v[114:115], v[154:155], v[184:185]
	s_waitcnt vmcnt(28)
	v_lshlrev_b32_e32 v156, 16, v142
	v_and_b32_e32 v157, 0xffff0000, v142
	v_lshlrev_b32_e32 v182, 16, v143
	v_and_b32_e32 v183, 0xffff0000, v143
	s_waitcnt vmcnt(27)
	v_and_b32_e32 v147, 0xffff0000, v124
	v_pk_add_f32 v[114:115], v[114:115], v[114:115] op_sel:[0,1] op_sel_hi:[1,0]
	v_add_f32_e32 v144, v156, v157
	v_add_f32_e32 v142, v182, v183
	v_lshlrev_b32_e32 v211, 16, v124
	v_lshlrev_b32_e32 v145, 16, v125
	v_and_b32_e32 v143, 0xffff0000, v125
	v_mov_b32_e32 v115, v147
	v_pk_add_f32 v[114:115], v[210:211], v[114:115]
	v_pk_add_f32 v[118:119], v[144:145], v[142:143]
	s_waitcnt vmcnt(26)
	v_lshlrev_b32_e32 v193, 16, v121
	v_lshlrev_b32_e32 v192, 16, v120
	v_and_b32_e32 v207, 0xffff0000, v121
	v_and_b32_e32 v206, 0xffff0000, v120
	v_pk_add_f32 v[114:115], v[114:115], v[118:119]
	v_pk_add_f32 v[118:119], v[192:193], v[206:207]
	s_waitcnt vmcnt(25)
	v_lshlrev_b32_e32 v194, 16, v116
	v_and_b32_e32 v195, 0xffff0000, v116
	v_lshlrev_b32_e32 v204, 16, v117
	v_and_b32_e32 v205, 0xffff0000, v117
	s_waitcnt vmcnt(24)
	v_lshlrev_b32_e32 v190, 16, v112
	v_and_b32_e32 v191, 0xffff0000, v112
	v_lshlrev_b32_e32 v189, 16, v113
	v_and_b32_e32 v187, 0xffff0000, v113
	v_pk_add_f32 v[112:113], v[114:115], v[114:115] op_sel:[0,1] op_sel_hi:[1,0]
	v_pk_add_f32 v[114:115], v[118:119], v[118:119] op_sel:[0,1] op_sel_hi:[1,0]
	v_add_f32_e32 v188, v194, v195
	v_add_f32_e32 v186, v204, v205
	v_mov_b32_e32 v113, v190
	v_mov_b32_e32 v115, v191
	v_pk_add_f32 v[112:113], v[112:113], v[114:115]
	v_pk_add_f32 v[114:115], v[188:189], v[186:187]
	s_movk_i32 s8, 0x7000
	v_pk_add_f32 v[112:113], v[112:113], v[114:115]
	v_add_co_u32_e32 v110, vcc, s8, v110
	v_add_f32_e32 v2, v112, v113
	v_addc_co_u32_e32 v111, vcc, 0, v111, vcc
	global_load_dwordx2 v[122:123], v[110:111], off
	global_load_dwordx2 v[124:125], v[110:111], off offset:512
	global_load_dwordx2 v[120:121], v[110:111], off offset:1024
	global_load_dwordx2 v[118:119], v[110:111], off offset:1536
	global_load_dwordx2 v[116:117], v[110:111], off offset:2048
	global_load_dwordx2 v[114:115], v[110:111], off offset:2560
	global_load_dwordx2 v[112:113], v[110:111], off offset:3072
	s_nop 0
	global_load_dwordx2 v[110:111], v[110:111], off offset:3584
	s_waitcnt lgkmcnt(0)
	s_nop 1
	v_add_f32_dpp v2, v2, v2 quad_perm:[1,0,3,2] row_mask:0xf bank_mask:0xf
	s_waitcnt lgkmcnt(0)
	s_nop 1
	v_add_f32_dpp v2, v2, v2 quad_perm:[2,3,0,1] row_mask:0xf bank_mask:0xf
	s_waitcnt lgkmcnt(0)
	s_nop 1
	v_add_f32_dpp v2, v2, v2 row_half_mirror row_mask:0xf bank_mask:0xf
	s_waitcnt lgkmcnt(0)
	s_nop 1
	v_add_f32_dpp v2, v2, v2 row_mirror row_mask:0xf bank_mask:0xf
	s_waitcnt lgkmcnt(0)
	v_mov_b32_e32 v142, v2
	s_nop 1
	v_permlane16_swap_b32_e32 v142, v2
	v_add_f32_e32 v2, v2, v142
	s_waitcnt lgkmcnt(0)
	v_mov_b32_e32 v142, v2
	s_nop 1
	v_permlane32_swap_b32_e32 v142, v2
	v_add_f32_e32 v142, v2, v142
	v_fmac_f32_e32 v148, 0xba000000, v142
	v_fmac_f32_e32 v150, 0xba000000, v142
	v_fmac_f32_e32 v152, 0xba000000, v142
	v_fmac_f32_e32 v208, 0xba000000, v142
	v_mul_f32_e32 v2, v150, v150
	v_mul_f32_e32 v144, v148, v148
	v_fmac_f32_e32 v2, v208, v208
	v_fmac_f32_e32 v144, v152, v152
	v_fmac_f32_e32 v149, 0xba000000, v142
	v_fmac_f32_e32 v151, 0xba000000, v142
	v_add_f32_e32 v2, v2, v144
	v_fmac_f32_e32 v153, 0xba000000, v142
	v_fmac_f32_e32 v209, 0xba000000, v142
	v_mul_f32_e32 v144, v151, v151
	v_mul_f32_e32 v146, v149, v149
	v_fmac_f32_e32 v144, v209, v209
	v_fmac_f32_e32 v146, v153, v153
	v_add_f32_e32 v144, v144, v146
	v_fmac_f32_e32 v185, 0xba000000, v142
	v_fmac_f32_e32 v184, 0xba000000, v142
	v_add_f32_e32 v2, v2, v144
	v_fmac_f32_e32 v155, 0xba000000, v142
	v_fmac_f32_e32 v154, 0xba000000, v142
	v_mul_f32_e32 v144, v184, v184
	v_mul_f32_e32 v146, v185, v185
	v_fmac_f32_e32 v144, v154, v154
	v_fmac_f32_e32 v146, v155, v155
	v_add_f32_e32 v144, v144, v146
	v_fmac_f32_e32 v183, 0xba000000, v142
	v_fmac_f32_e32 v157, 0xba000000, v142
	v_add_f32_e32 v2, v144, v2
	v_fmac_f32_e32 v182, 0xba000000, v142
	v_fmac_f32_e32 v156, 0xba000000, v142
	v_mul_f32_e32 v144, v157, v157
	v_mul_f32_e32 v146, v183, v183
	v_fmac_f32_e32 v144, v156, v156
	v_fmac_f32_e32 v146, v182, v182
	v_add_f32_e32 v144, v144, v146
	v_fmac_f32_e32 v143, 0xba000000, v142
	v_fmac_f32_e32 v147, 0xba000000, v142
	v_add_f32_e32 v2, v144, v2
	v_fmac_f32_e32 v145, 0xba000000, v142
	v_fmac_f32_e32 v211, 0xba000000, v142
	v_mul_f32_e32 v144, v147, v147
	v_mul_f32_e32 v146, v143, v143
	v_fmac_f32_e32 v144, v211, v211
	v_fmac_f32_e32 v146, v145, v145
	v_add_f32_e32 v144, v144, v146
	v_fmac_f32_e32 v207, 0xba000000, v142
	v_fmac_f32_e32 v206, 0xba000000, v142
	v_add_f32_e32 v2, v144, v2
	v_fmac_f32_e32 v193, 0xba000000, v142
	v_fmac_f32_e32 v192, 0xba000000, v142
	v_mul_f32_e32 v144, v206, v206
	v_mul_f32_e32 v146, v207, v207
	v_fmac_f32_e32 v144, v192, v192
	v_fmac_f32_e32 v146, v193, v193
	v_add_f32_e32 v144, v144, v146
	v_fmac_f32_e32 v205, 0xba000000, v142
	v_fmac_f32_e32 v195, 0xba000000, v142
	v_add_f32_e32 v2, v144, v2
	v_fmac_f32_e32 v204, 0xba000000, v142
	v_fmac_f32_e32 v194, 0xba000000, v142
	v_mul_f32_e32 v144, v195, v195
	v_mul_f32_e32 v146, v205, v205
	v_fmac_f32_e32 v144, v194, v194
	v_fmac_f32_e32 v146, v204, v204
	v_add_f32_e32 v144, v144, v146
	v_fmac_f32_e32 v187, 0xba000000, v142
	v_fmac_f32_e32 v191, 0xba000000, v142
	v_add_f32_e32 v2, v144, v2
	v_fmac_f32_e32 v189, 0xba000000, v142
	v_fmac_f32_e32 v190, 0xba000000, v142
	v_mul_f32_e32 v144, v191, v191
	v_mul_f32_e32 v146, v187, v187
	v_fmac_f32_e32 v144, v190, v190
	v_fmac_f32_e32 v146, v189, v189
	v_add_f32_e32 v144, v144, v146
	v_add_f32_e32 v2, v144, v2
	s_waitcnt lgkmcnt(0)
	s_nop 1
	v_add_f32_dpp v2, v2, v2 quad_perm:[1,0,3,2] row_mask:0xf bank_mask:0xf
	s_waitcnt lgkmcnt(0)
	s_nop 1
	v_add_f32_dpp v2, v2, v2 quad_perm:[2,3,0,1] row_mask:0xf bank_mask:0xf
	s_waitcnt lgkmcnt(0)
	s_nop 1
	v_add_f32_dpp v2, v2, v2 row_half_mirror row_mask:0xf bank_mask:0xf
	s_waitcnt lgkmcnt(0)
	s_nop 1
	v_add_f32_dpp v2, v2, v2 row_mirror row_mask:0xf bank_mask:0xf
	s_waitcnt lgkmcnt(0)
	v_mov_b32_e32 v144, v2
	s_nop 1
	v_permlane16_swap_b32_e32 v144, v2
	v_add_f32_e32 v2, v2, v144
	s_waitcnt lgkmcnt(0)
	v_mov_b32_e32 v144, v2
	s_nop 1
	v_permlane32_swap_b32_e32 v144, v2
	v_add_f32_e32 v2, v2, v144
	v_fmamk_f32 v2, v2, 0x3a000000, v217
	v_cmp_gt_f32_e32 vcc, s87, v2
	v_mul_f32_e32 v144, 0x4f800000, v2
	s_nop 0
	v_cndmask_b32_e32 v2, v2, v144, vcc
	v_sqrt_f32_e32 v144, v2
	s_nop 0
	v_add_u32_e32 v146, -1, v144
	v_fma_f32 v186, -v146, v144, v2
	v_cmp_ge_f32_e64 s[8:9], 0, v186
	v_add_u32_e32 v186, 1, v144
	s_nop 0
	v_cndmask_b32_e64 v146, v144, v146, s[8:9]
	v_fma_f32 v144, -v186, v144, v2
	v_cmp_lt_f32_e64 s[8:9], 0, v144
	s_nop 1
	v_cndmask_b32_e64 v144, v146, v186, s[8:9]
	v_mul_f32_e32 v146, 0x37800000, v144
	v_cndmask_b32_e32 v144, v144, v146, vcc
	v_cmp_class_f32_e32 vcc, v2, v218
	s_nop 1
	v_cndmask_b32_e32 v2, v144, v2, vcc
	v_div_scale_f32 v144, s[8:9], v2, v2, 1.0
	v_rcp_f32_e32 v146, v144
	s_nop 0
	v_fma_f32 v186, -v144, v146, 1.0
	v_fmac_f32_e32 v146, v186, v146
	v_div_scale_f32 v186, vcc, 1.0, v2, 1.0
	v_mul_f32_e32 v188, v186, v146
	v_fma_f32 v210, -v144, v188, v186
	v_fmac_f32_e32 v188, v210, v146
	v_fma_f32 v144, -v144, v188, v186
	v_div_fmas_f32 v144, v144, v146, v188
	v_div_fixup_f32 v2, v144, v2, 1.0
	s_and_saveexec_b64 s[8:9], s[4:5]
	s_add_i32 s10, s78, 0
	v_mul_f32_e32 v212, 0x3a000000, v142
	v_mov_b32_e32 v213, v2
	v_mov_b32_e32 v142, s10
	ds_write_b64 v142, v[212:213] offset:33832
	s_or_b64 exec, exec, s[8:9]
	v_mov_b32_e32 v212, v208
	v_mov_b32_e32 v213, v150
	v_mov_b32_e32 v214, v152
	v_mov_b32_e32 v215, v148
	v_pk_mul_f32 v[214:215], v[214:215], v[2:3] op_sel_hi:[1,0]
	v_pk_mul_f32 v[212:213], v[212:213], v[2:3] op_sel_hi:[1,0]
	v_mov_b32_e32 v150, v209
	v_pk_fma_f32 v[214:215], v[104:105], v[214:215], v[108:109]
	v_pk_fma_f32 v[212:213], v[102:103], v[212:213], v[106:107]
	s_movk_i32 s8, 0x5000
	v_cvt_pk_bf16_f32 v212, v212, v213
	v_cvt_pk_bf16_f32 v213, v214, v215
	v_add_co_u32_e32 v214, vcc, s8, v4
	v_mov_b32_e32 v148, v153
	v_pk_mul_f32 v[150:151], v[150:151], v[2:3] op_sel_hi:[1,0]
	v_addc_co_u32_e32 v215, vcc, 0, v5, vcc
	v_pk_mul_f32 v[148:149], v[148:149], v[2:3] op_sel_hi:[1,0]
	v_pk_fma_f32 v[150:151], v[94:95], v[150:151], v[98:99]
	v_mov_b32_e32 v208, v154
	v_mov_b32_e32 v209, v184
	global_store_dwordx2 v[214:215], v[212:213], off
	v_pk_fma_f32 v[148:149], v[96:97], v[148:149], v[100:101]
	v_cvt_pk_bf16_f32 v150, v150, v151
	v_mov_b32_e32 v184, v155
	v_cvt_pk_bf16_f32 v151, v148, v149
	global_store_dwordx2 v[214:215], v[150:151], off offset:512
	v_pk_mul_f32 v[150:151], v[208:209], v[2:3] op_sel_hi:[1,0]
	v_pk_mul_f32 v[148:149], v[184:185], v[2:3] op_sel_hi:[1,0]
	v_pk_fma_f32 v[150:151], v[86:87], v[150:151], v[90:91]
	v_mov_b32_e32 v146, v211
	v_pk_fma_f32 v[148:149], v[88:89], v[148:149], v[92:93]
	v_cvt_pk_bf16_f32 v150, v150, v151
	v_mov_b32_e32 v142, v145
	v_cvt_pk_bf16_f32 v151, v148, v149
	global_store_dwordx2 v[214:215], v[150:151], off offset:1024
	v_pk_mul_f32 v[150:151], v[156:157], v[2:3] op_sel_hi:[1,0]
	v_pk_mul_f32 v[144:145], v[146:147], v[2:3] op_sel_hi:[1,0]
	v_pk_mul_f32 v[148:149], v[182:183], v[2:3] op_sel_hi:[1,0]
	v_pk_fma_f32 v[150:151], v[78:79], v[150:151], v[82:83]
	v_pk_mul_f32 v[142:143], v[142:143], v[2:3] op_sel_hi:[1,0]
	v_pk_fma_f32 v[144:145], v[70:71], v[144:145], v[74:75]
	v_mov_b32_e32 v210, v192
	v_mov_b32_e32 v211, v206
	v_pk_fma_f32 v[148:149], v[80:81], v[148:149], v[84:85]
	v_cvt_pk_bf16_f32 v150, v150, v151
	v_pk_fma_f32 v[142:143], v[72:73], v[142:143], v[76:77]
	v_cvt_pk_bf16_f32 v151, v148, v149
	global_store_dwordx2 v[214:215], v[150:151], off offset:1536
	v_cvt_pk_bf16_f32 v144, v144, v145
	v_cvt_pk_bf16_f32 v145, v142, v143
	global_store_dwordx2 v[214:215], v[144:145], off offset:2048
	v_mov_b32_e32 v206, v193
	v_pk_mul_f32 v[144:145], v[210:211], v[2:3] op_sel_hi:[1,0]
	v_pk_mul_f32 v[142:143], v[206:207], v[2:3] op_sel_hi:[1,0]
	v_pk_fma_f32 v[144:145], v[62:63], v[144:145], v[66:67]
	v_pk_fma_f32 v[142:143], v[64:65], v[142:143], v[68:69]
	v_cvt_pk_bf16_f32 v144, v144, v145
	v_mov_b32_e32 v186, v189
	v_cvt_pk_bf16_f32 v145, v142, v143
	global_store_dwordx2 v[214:215], v[144:145], off offset:2560
	v_pk_mul_f32 v[144:145], v[194:195], v[2:3] op_sel_hi:[1,0]
	v_pk_mul_f32 v[142:143], v[204:205], v[2:3] op_sel_hi:[1,0]
	v_pk_fma_f32 v[144:145], v[54:55], v[144:145], v[58:59]
	v_pk_fma_f32 v[142:143], v[56:57], v[142:143], v[60:61]
	v_cvt_pk_bf16_f32 v144, v144, v145
	s_waitcnt vmcnt(27)
	v_and_b32_e32 v151, 0xffff0000, v137
	v_cvt_pk_bf16_f32 v145, v142, v143
	global_store_dwordx2 v[214:215], v[144:145], off offset:3072
	v_pk_mul_f32 v[144:145], v[190:191], v[2:3] op_sel_hi:[1,0]
	v_pk_mul_f32 v[142:143], v[186:187], v[2:3] op_sel_hi:[1,0]
	v_pk_fma_f32 v[144:145], v[46:47], v[144:145], v[50:51]
	v_pk_fma_f32 v[142:143], v[48:49], v[142:143], v[52:53]
	v_cvt_pk_bf16_f32 v144, v144, v145
	v_lshlrev_b32_e32 v187, 16, v140
	v_cvt_pk_bf16_f32 v145, v142, v143
	global_store_dwordx2 v[214:215], v[144:145], off offset:3584
	v_lshlrev_b32_e32 v186, 16, v138
	v_and_b32_e32 v143, 0xffff0000, v140
	v_and_b32_e32 v142, 0xffff0000, v138
	v_lshlrev_b32_e32 v145, 16, v141
	v_lshlrev_b32_e32 v144, 16, v139
	v_and_b32_e32 v141, 0xffff0000, v141
	v_and_b32_e32 v140, 0xffff0000, v139
	v_pk_add_f32 v[146:147], v[186:187], v[142:143]
	v_pk_add_f32 v[138:139], v[144:145], v[140:141]
	v_and_b32_e32 v150, 0xffff0000, v136
	v_pk_add_f32 v[138:139], v[146:147], v[138:139]
	v_lshlrev_b32_e32 v147, 16, v137
	v_lshlrev_b32_e32 v146, 16, v136
	v_add_f32_e32 v2, 0, v138
	v_pk_add_f32 v[154:155], v[146:147], v[150:151]
	v_add_f32_e32 v188, v2, v139
	s_waitcnt vmcnt(28)
	v_lshlrev_b32_e32 v148, 16, v134
	v_and_b32_e32 v149, 0xffff0000, v134
	v_lshlrev_b32_e32 v152, 16, v135
	v_and_b32_e32 v153, 0xffff0000, v135
	s_waitcnt vmcnt(27)
	v_lshlrev_b32_e32 v189, 16, v132
	v_and_b32_e32 v139, 0xffff0000, v132
	v_lshlrev_b32_e32 v135, 16, v133
	v_and_b32_e32 v137, 0xffff0000, v133
	v_pk_add_f32 v[132:133], v[154:155], v[154:155] op_sel:[0,1] op_sel_hi:[1,0]
	v_add_f32_e32 v134, v148, v149
	v_add_f32_e32 v136, v152, v153
	v_mov_b32_e32 v133, v139
	v_pk_add_f32 v[132:133], v[188:189], v[132:133]
	v_pk_add_f32 v[154:155], v[134:135], v[136:137]
	s_waitcnt vmcnt(26)
	v_and_b32_e32 v183, 0xffff0000, v131
	v_pk_add_f32 v[190:191], v[132:133], v[154:155]
	v_lshlrev_b32_e32 v155, 16, v131
	v_lshlrev_b32_e32 v154, 16, v130
	v_and_b32_e32 v182, 0xffff0000, v130
	v_pk_add_f32 v[192:193], v[154:155], v[182:183]
	s_waitcnt vmcnt(25)
	v_lshlrev_b32_e32 v156, 16, v128
	v_and_b32_e32 v157, 0xffff0000, v128
	v_lshlrev_b32_e32 v184, 16, v129
	v_and_b32_e32 v185, 0xffff0000, v129
	s_waitcnt vmcnt(24)
	v_lshlrev_b32_e32 v132, 16, v126
	v_and_b32_e32 v133, 0xffff0000, v126
	v_lshlrev_b32_e32 v129, 16, v127
	v_and_b32_e32 v131, 0xffff0000, v127
	v_pk_add_f32 v[126:127], v[190:191], v[190:191] op_sel:[0,1] op_sel_hi:[1,0]
	v_pk_add_f32 v[190:191], v[192:193], v[192:193] op_sel:[0,1] op_sel_hi:[1,0]
	v_add_f32_e32 v128, v156, v157
	v_add_f32_e32 v130, v184, v185
	v_mov_b32_e32 v127, v132
	v_mov_b32_e32 v191, v133
	v_pk_add_f32 v[126:127], v[126:127], v[190:191]
	v_pk_add_f32 v[190:191], v[128:129], v[130:131]
	s_nop 0
	v_pk_add_f32 v[126:127], v[126:127], v[190:191]
	s_nop 0
	v_add_f32_e32 v2, v126, v127
	s_waitcnt lgkmcnt(0)
	s_nop 1
	v_add_f32_dpp v2, v2, v2 quad_perm:[1,0,3,2] row_mask:0xf bank_mask:0xf
	s_waitcnt lgkmcnt(0)
	s_nop 1
	v_add_f32_dpp v2, v2, v2 quad_perm:[2,3,0,1] row_mask:0xf bank_mask:0xf
	s_waitcnt lgkmcnt(0)
	s_nop 1
	v_add_f32_dpp v2, v2, v2 row_half_mirror row_mask:0xf bank_mask:0xf
	s_waitcnt lgkmcnt(0)
	s_nop 1
	v_add_f32_dpp v2, v2, v2 row_mirror row_mask:0xf bank_mask:0xf
	s_waitcnt lgkmcnt(0)
	v_mov_b32_e32 v126, v2
	s_nop 1
	v_permlane16_swap_b32_e32 v126, v2
	v_add_f32_e32 v2, v2, v126
	s_waitcnt lgkmcnt(0)
	v_mov_b32_e32 v126, v2
	s_nop 1
	v_permlane32_swap_b32_e32 v126, v2
	v_add_f32_e32 v126, v2, v126
	v_fmac_f32_e32 v140, 0xba000000, v126
	v_fmac_f32_e32 v142, 0xba000000, v126
	v_fmac_f32_e32 v144, 0xba000000, v126
	v_fmac_f32_e32 v186, 0xba000000, v126
	v_mul_f32_e32 v2, v142, v142
	v_mul_f32_e32 v127, v140, v140
	v_fmac_f32_e32 v2, v186, v186
	v_fmac_f32_e32 v127, v144, v144
	v_fmac_f32_e32 v141, 0xba000000, v126
	v_fmac_f32_e32 v143, 0xba000000, v126
	v_add_f32_e32 v2, v2, v127
	v_fmac_f32_e32 v145, 0xba000000, v126
	v_fmac_f32_e32 v187, 0xba000000, v126
	v_mul_f32_e32 v127, v143, v143
	v_mul_f32_e32 v128, v141, v141
	v_fmac_f32_e32 v127, v187, v187
	v_fmac_f32_e32 v128, v145, v145
	v_add_f32_e32 v127, v127, v128
	v_fmac_f32_e32 v151, 0xba000000, v126
	v_fmac_f32_e32 v150, 0xba000000, v126
	v_add_f32_e32 v2, v2, v127
	v_fmac_f32_e32 v147, 0xba000000, v126
	v_fmac_f32_e32 v146, 0xba000000, v126
	v_mul_f32_e32 v127, v150, v150
	v_mul_f32_e32 v128, v151, v151
	v_fmac_f32_e32 v127, v146, v146
	v_fmac_f32_e32 v128, v147, v147
	v_add_f32_e32 v127, v127, v128
	v_fmac_f32_e32 v153, 0xba000000, v126
	v_fmac_f32_e32 v149, 0xba000000, v126
	v_add_f32_e32 v2, v127, v2
	v_fmac_f32_e32 v152, 0xba000000, v126
	v_fmac_f32_e32 v148, 0xba000000, v126
	v_mul_f32_e32 v127, v149, v149
	v_mul_f32_e32 v128, v153, v153
	v_fmac_f32_e32 v127, v148, v148
	v_fmac_f32_e32 v128, v152, v152
	v_add_f32_e32 v127, v127, v128
	v_fmac_f32_e32 v137, 0xba000000, v126
	v_fmac_f32_e32 v139, 0xba000000, v126
	v_add_f32_e32 v2, v127, v2
	v_fmac_f32_e32 v135, 0xba000000, v126
	v_fmac_f32_e32 v189, 0xba000000, v126
	v_mul_f32_e32 v127, v139, v139
	v_mul_f32_e32 v128, v137, v137
	v_fmac_f32_e32 v127, v189, v189
	v_fmac_f32_e32 v128, v135, v135
	v_add_f32_e32 v127, v127, v128
	v_fmac_f32_e32 v183, 0xba000000, v126
	v_fmac_f32_e32 v182, 0xba000000, v126
	v_add_f32_e32 v2, v127, v2
	v_fmac_f32_e32 v155, 0xba000000, v126
	v_fmac_f32_e32 v154, 0xba000000, v126
	v_mul_f32_e32 v127, v182, v182
	v_mul_f32_e32 v128, v183, v183
	v_fmac_f32_e32 v127, v154, v154
	v_fmac_f32_e32 v128, v155, v155
	v_add_f32_e32 v127, v127, v128
	v_fmac_f32_e32 v185, 0xba000000, v126
	v_fmac_f32_e32 v157, 0xba000000, v126
	v_add_f32_e32 v2, v127, v2
	v_fmac_f32_e32 v184, 0xba000000, v126
	v_fmac_f32_e32 v156, 0xba000000, v126
	v_mul_f32_e32 v127, v157, v157
	v_mul_f32_e32 v128, v185, v185
	v_fmac_f32_e32 v127, v156, v156
	v_fmac_f32_e32 v128, v184, v184
	v_add_f32_e32 v127, v127, v128
	v_fmac_f32_e32 v131, 0xba000000, v126
	v_fmac_f32_e32 v133, 0xba000000, v126
	v_add_f32_e32 v2, v127, v2
	v_fmac_f32_e32 v129, 0xba000000, v126
	v_fmac_f32_e32 v132, 0xba000000, v126
	v_mul_f32_e32 v127, v133, v133
	v_mul_f32_e32 v128, v131, v131
	v_fmac_f32_e32 v127, v132, v132
	v_fmac_f32_e32 v128, v129, v129
	v_add_f32_e32 v127, v127, v128
	v_add_f32_e32 v2, v127, v2
	s_waitcnt lgkmcnt(0)
	s_nop 1
	v_add_f32_dpp v2, v2, v2 quad_perm:[1,0,3,2] row_mask:0xf bank_mask:0xf
	s_waitcnt lgkmcnt(0)
	s_nop 1
	v_add_f32_dpp v2, v2, v2 quad_perm:[2,3,0,1] row_mask:0xf bank_mask:0xf
	s_waitcnt lgkmcnt(0)
	s_nop 1
	v_add_f32_dpp v2, v2, v2 row_half_mirror row_mask:0xf bank_mask:0xf
	s_waitcnt lgkmcnt(0)
	s_nop 1
	v_add_f32_dpp v2, v2, v2 row_mirror row_mask:0xf bank_mask:0xf
	s_waitcnt lgkmcnt(0)
	v_mov_b32_e32 v127, v2
	s_nop 1
	v_permlane16_swap_b32_e32 v127, v2
	v_add_f32_e32 v2, v2, v127
	s_waitcnt lgkmcnt(0)
	v_mov_b32_e32 v127, v2
	s_nop 1
	v_permlane32_swap_b32_e32 v127, v2
	v_add_f32_e32 v2, v2, v127
	v_fmamk_f32 v2, v2, 0x3a000000, v217
	v_cmp_gt_f32_e32 vcc, s87, v2
	v_mul_f32_e32 v127, 0x4f800000, v2
	s_nop 0
	v_cndmask_b32_e32 v2, v2, v127, vcc
	v_sqrt_f32_e32 v127, v2
	s_nop 0
	v_add_u32_e32 v128, -1, v127
	v_fma_f32 v130, -v128, v127, v2
	v_cmp_ge_f32_e64 s[8:9], 0, v130
	v_add_u32_e32 v130, 1, v127
	s_nop 0
	v_cndmask_b32_e64 v128, v127, v128, s[8:9]
	v_fma_f32 v127, -v130, v127, v2
	v_cmp_lt_f32_e64 s[8:9], 0, v127
	s_nop 1
	v_cndmask_b32_e64 v127, v128, v130, s[8:9]
	v_mul_f32_e32 v128, 0x37800000, v127
	v_cndmask_b32_e32 v127, v127, v128, vcc
	v_cmp_class_f32_e32 vcc, v2, v218
	s_nop 1
	v_cndmask_b32_e32 v2, v127, v2, vcc
	v_div_scale_f32 v127, s[8:9], v2, v2, 1.0
	v_rcp_f32_e32 v128, v127
	s_nop 0
	v_fma_f32 v130, -v127, v128, 1.0
	v_fmac_f32_e32 v128, v130, v128
	v_div_scale_f32 v130, vcc, 1.0, v2, 1.0
	v_mul_f32_e32 v134, v130, v128
	v_fma_f32 v136, -v127, v134, v130
	v_fmac_f32_e32 v134, v136, v128
	v_fma_f32 v127, -v127, v134, v130
	v_div_fmas_f32 v127, v127, v128, v134
	v_div_fixup_f32 v2, v127, v2, 1.0
	s_and_saveexec_b64 s[8:9], s[4:5]
	s_add_i32 s10, s78, 0
	v_mul_f32_e32 v126, 0x3a000000, v126
	v_mov_b32_e32 v127, v2
	v_mov_b32_e32 v128, s10
	ds_write_b64 v128, v[126:127] offset:33840
	s_or_b64 exec, exec, s[8:9]
	v_mov_b32_e32 v126, v186
	v_mov_b32_e32 v127, v142
	v_mov_b32_e32 v190, v144
	v_mov_b32_e32 v191, v140
	v_pk_mul_f32 v[190:191], v[190:191], v[2:3] op_sel_hi:[1,0]
	v_pk_mul_f32 v[126:127], v[126:127], v[2:3] op_sel_hi:[1,0]
	v_pk_fma_f32 v[190:191], v[104:105], v[190:191], v[108:109]
	v_pk_fma_f32 v[126:127], v[102:103], v[126:127], v[106:107]
	s_movk_i32 s8, 0x6000
	v_cvt_pk_bf16_f32 v126, v126, v127
	v_cvt_pk_bf16_f32 v127, v190, v191
	v_add_co_u32_e32 v190, vcc, s8, v4
	v_mov_b32_e32 v142, v187
	s_nop 0
	v_addc_co_u32_e32 v191, vcc, 0, v5, vcc
	v_mov_b32_e32 v140, v145
	global_store_dwordx2 v[190:191], v[126:127], off
	v_pk_mul_f32 v[126:127], v[140:141], v[2:3] op_sel_hi:[1,0]
	v_pk_mul_f32 v[140:141], v[142:143], v[2:3] op_sel_hi:[1,0]
	v_mov_b32_e32 v186, v146
	v_pk_fma_f32 v[140:141], v[94:95], v[140:141], v[98:99]
	v_mov_b32_e32 v187, v150
	v_pk_fma_f32 v[126:127], v[96:97], v[126:127], v[100:101]
	v_cvt_pk_bf16_f32 v140, v140, v141
	v_mov_b32_e32 v150, v147
	v_cvt_pk_bf16_f32 v141, v126, v127
	global_store_dwordx2 v[190:191], v[140:141], off offset:512
	v_pk_mul_f32 v[140:141], v[186:187], v[2:3] op_sel_hi:[1,0]
	v_pk_mul_f32 v[126:127], v[150:151], v[2:3] op_sel_hi:[1,0]
	v_pk_fma_f32 v[140:141], v[86:87], v[140:141], v[90:91]
	v_pk_fma_f32 v[126:127], v[88:89], v[126:127], v[92:93]
	v_cvt_pk_bf16_f32 v140, v140, v141
	v_mov_b32_e32 v138, v189
	v_cvt_pk_bf16_f32 v141, v126, v127
	global_store_dwordx2 v[190:191], v[140:141], off offset:1024
	v_pk_mul_f32 v[126:127], v[152:153], v[2:3] op_sel_hi:[1,0]
	v_pk_mul_f32 v[140:141], v[148:149], v[2:3] op_sel_hi:[1,0]
	v_pk_fma_f32 v[126:127], v[80:81], v[126:127], v[84:85]
	v_pk_fma_f32 v[140:141], v[78:79], v[140:141], v[82:83]
	v_mov_b32_e32 v136, v135
	v_pk_mul_f32 v[134:135], v[138:139], v[2:3] op_sel_hi:[1,0]
	v_cvt_pk_bf16_f32 v140, v140, v141
	v_cvt_pk_bf16_f32 v141, v126, v127
	v_pk_mul_f32 v[126:127], v[136:137], v[2:3] op_sel_hi:[1,0]
	v_pk_fma_f32 v[134:135], v[70:71], v[134:135], v[74:75]
	v_mov_b32_e32 v188, v154
	v_mov_b32_e32 v189, v182
	global_store_dwordx2 v[190:191], v[140:141], off offset:1536
	v_pk_fma_f32 v[126:127], v[72:73], v[126:127], v[76:77]
	v_cvt_pk_bf16_f32 v134, v134, v135
	v_mov_b32_e32 v182, v155
	v_cvt_pk_bf16_f32 v135, v126, v127
	global_store_dwordx2 v[190:191], v[134:135], off offset:2048
	v_pk_mul_f32 v[134:135], v[188:189], v[2:3] op_sel_hi:[1,0]
	v_pk_mul_f32 v[126:127], v[182:183], v[2:3] op_sel_hi:[1,0]
	v_pk_fma_f32 v[134:135], v[62:63], v[134:135], v[66:67]
	v_pk_fma_f32 v[126:127], v[64:65], v[126:127], v[68:69]
	v_cvt_pk_bf16_f32 v134, v134, v135
	v_mov_b32_e32 v130, v129
	v_cvt_pk_bf16_f32 v135, v126, v127
	global_store_dwordx2 v[190:191], v[134:135], off offset:2560
	v_pk_mul_f32 v[126:127], v[184:185], v[2:3] op_sel_hi:[1,0]
	v_pk_mul_f32 v[134:135], v[156:157], v[2:3] op_sel_hi:[1,0]
	v_pk_fma_f32 v[126:127], v[56:57], v[126:127], v[60:61]
	v_pk_fma_f32 v[134:135], v[54:55], v[134:135], v[58:59]
	v_pk_mul_f32 v[128:129], v[132:133], v[2:3] op_sel_hi:[1,0]
	v_cvt_pk_bf16_f32 v134, v134, v135
	v_cvt_pk_bf16_f32 v135, v126, v127
	v_pk_mul_f32 v[126:127], v[130:131], v[2:3] op_sel_hi:[1,0]
	v_pk_fma_f32 v[128:129], v[46:47], v[128:129], v[50:51]
	v_pk_fma_f32 v[126:127], v[48:49], v[126:127], v[52:53]
	s_waitcnt vmcnt(20)
	v_lshlrev_b32_e32 v147, 16, v124
	v_lshlrev_b32_e32 v146, 16, v122
	v_and_b32_e32 v137, 0xffff0000, v124
	v_and_b32_e32 v136, 0xffff0000, v122
	v_lshlrev_b32_e32 v143, 16, v125
	v_lshlrev_b32_e32 v142, 16, v123
	v_and_b32_e32 v145, 0xffff0000, v125
	v_and_b32_e32 v144, 0xffff0000, v123
	global_store_dwordx2 v[190:191], v[134:135], off offset:3072
	v_cvt_pk_bf16_f32 v128, v128, v129
	v_cvt_pk_bf16_f32 v129, v126, v127
	v_pk_add_f32 v[126:127], v[146:147], v[136:137]
	v_pk_add_f32 v[122:123], v[142:143], v[144:145]
	s_waitcnt vmcnt(20)
	v_lshlrev_b32_e32 v139, 16, v121
	v_pk_add_f32 v[122:123], v[126:127], v[122:123]
	v_lshlrev_b32_e32 v138, 16, v120
	v_and_b32_e32 v141, 0xffff0000, v121
	v_and_b32_e32 v140, 0xffff0000, v120
	v_add_f32_e32 v2, 0, v122
	v_pk_add_f32 v[120:121], v[138:139], v[140:141]
	v_add_f32_e32 v148, v2, v123
	s_waitcnt vmcnt(19)
	v_lshlrev_b32_e32 v132, 16, v118
	v_and_b32_e32 v133, 0xffff0000, v118
	v_lshlrev_b32_e32 v134, 16, v119
	v_and_b32_e32 v135, 0xffff0000, v119
	s_waitcnt vmcnt(18)
	v_lshlrev_b32_e32 v149, 16, v116
	v_and_b32_e32 v127, 0xffff0000, v116
	v_lshlrev_b32_e32 v123, 16, v117
	v_and_b32_e32 v125, 0xffff0000, v117
	v_pk_add_f32 v[116:117], v[120:121], v[120:121] op_sel:[0,1] op_sel_hi:[1,0]
	v_add_f32_e32 v122, v132, v133
	v_add_f32_e32 v124, v134, v135
	v_mov_b32_e32 v117, v127
	global_store_dwordx2 v[190:191], v[128:129], off offset:3584
	v_pk_add_f32 v[116:117], v[148:149], v[116:117]
	v_pk_add_f32 v[118:119], v[122:123], v[124:125]
	s_waitcnt vmcnt(18)
	v_lshlrev_b32_e32 v129, 16, v115
	v_lshlrev_b32_e32 v128, 16, v114
	v_and_b32_e32 v131, 0xffff0000, v115
	v_and_b32_e32 v130, 0xffff0000, v114
	v_pk_add_f32 v[150:151], v[116:117], v[118:119]
	v_pk_add_f32 v[152:153], v[128:129], v[130:131]
	s_waitcnt vmcnt(17)
	v_lshlrev_b32_e32 v118, 16, v112
	v_and_b32_e32 v119, 0xffff0000, v112
	v_lshlrev_b32_e32 v120, 16, v113
	v_and_b32_e32 v121, 0xffff0000, v113
	s_waitcnt vmcnt(16)
	v_lshlrev_b32_e32 v116, 16, v110
	v_and_b32_e32 v117, 0xffff0000, v110
	v_lshlrev_b32_e32 v113, 16, v111
	v_and_b32_e32 v115, 0xffff0000, v111
	v_pk_add_f32 v[110:111], v[150:151], v[150:151] op_sel:[0,1] op_sel_hi:[1,0]
	v_pk_add_f32 v[150:151], v[152:153], v[152:153] op_sel:[0,1] op_sel_hi:[1,0]
	v_add_f32_e32 v112, v118, v119
	v_add_f32_e32 v114, v120, v121
	v_mov_b32_e32 v111, v116
	v_mov_b32_e32 v151, v117
	v_pk_add_f32 v[110:111], v[110:111], v[150:151]
	v_pk_add_f32 v[150:151], v[112:113], v[114:115]
	s_nop 0
	v_pk_add_f32 v[110:111], v[110:111], v[150:151]
	s_nop 0
	v_add_f32_e32 v2, v110, v111
	s_waitcnt lgkmcnt(0)
	s_nop 1
	v_add_f32_dpp v2, v2, v2 quad_perm:[1,0,3,2] row_mask:0xf bank_mask:0xf
	s_waitcnt lgkmcnt(0)
	s_nop 1
	v_add_f32_dpp v2, v2, v2 quad_perm:[2,3,0,1] row_mask:0xf bank_mask:0xf
	s_waitcnt lgkmcnt(0)
	s_nop 1
	v_add_f32_dpp v2, v2, v2 row_half_mirror row_mask:0xf bank_mask:0xf
	s_waitcnt lgkmcnt(0)
	s_nop 1
	v_add_f32_dpp v2, v2, v2 row_mirror row_mask:0xf bank_mask:0xf
	s_waitcnt lgkmcnt(0)
	v_mov_b32_e32 v110, v2
	s_nop 1
	v_permlane16_swap_b32_e32 v110, v2
	v_add_f32_e32 v2, v2, v110
	s_waitcnt lgkmcnt(0)
	v_mov_b32_e32 v110, v2
	s_nop 1
	v_permlane32_swap_b32_e32 v110, v2
	v_add_f32_e32 v110, v2, v110
	v_fmac_f32_e32 v144, 0xba000000, v110
	v_fmac_f32_e32 v136, 0xba000000, v110
	v_fmac_f32_e32 v142, 0xba000000, v110
	v_fmac_f32_e32 v146, 0xba000000, v110
	v_mul_f32_e32 v2, v136, v136
	v_mul_f32_e32 v111, v144, v144
	v_fmac_f32_e32 v2, v146, v146
	v_fmac_f32_e32 v111, v142, v142
	v_fmac_f32_e32 v145, 0xba000000, v110
	v_fmac_f32_e32 v137, 0xba000000, v110
	v_add_f32_e32 v2, v2, v111
	v_fmac_f32_e32 v143, 0xba000000, v110
	v_fmac_f32_e32 v147, 0xba000000, v110
	v_mul_f32_e32 v111, v137, v137
	v_mul_f32_e32 v112, v145, v145
	v_fmac_f32_e32 v111, v147, v147
	v_fmac_f32_e32 v112, v143, v143
	v_add_f32_e32 v111, v111, v112
	v_fmac_f32_e32 v141, 0xba000000, v110
	v_fmac_f32_e32 v140, 0xba000000, v110
	v_add_f32_e32 v2, v2, v111
	v_fmac_f32_e32 v139, 0xba000000, v110
	v_fmac_f32_e32 v138, 0xba000000, v110
	v_mul_f32_e32 v111, v140, v140
	v_mul_f32_e32 v112, v141, v141
	v_fmac_f32_e32 v111, v138, v138
	v_fmac_f32_e32 v112, v139, v139
	v_add_f32_e32 v111, v111, v112
	v_fmac_f32_e32 v135, 0xba000000, v110
	v_fmac_f32_e32 v133, 0xba000000, v110
	v_add_f32_e32 v2, v111, v2
	v_fmac_f32_e32 v134, 0xba000000, v110
	v_fmac_f32_e32 v132, 0xba000000, v110
	v_mul_f32_e32 v111, v133, v133
	v_mul_f32_e32 v112, v135, v135
	v_fmac_f32_e32 v111, v132, v132
	v_fmac_f32_e32 v112, v134, v134
	v_add_f32_e32 v111, v111, v112
	v_fmac_f32_e32 v125, 0xba000000, v110
	v_fmac_f32_e32 v127, 0xba000000, v110
	v_add_f32_e32 v2, v111, v2
	v_fmac_f32_e32 v123, 0xba000000, v110
	v_fmac_f32_e32 v149, 0xba000000, v110
	v_mul_f32_e32 v111, v127, v127
	v_mul_f32_e32 v112, v125, v125
	v_fmac_f32_e32 v111, v149, v149
	v_fmac_f32_e32 v112, v123, v123
	v_add_f32_e32 v111, v111, v112
	v_fmac_f32_e32 v131, 0xba000000, v110
	v_fmac_f32_e32 v130, 0xba000000, v110
	v_add_f32_e32 v2, v111, v2
	v_fmac_f32_e32 v129, 0xba000000, v110
	v_fmac_f32_e32 v128, 0xba000000, v110
	v_mul_f32_e32 v111, v130, v130
	v_mul_f32_e32 v112, v131, v131
	v_fmac_f32_e32 v111, v128, v128
	v_fmac_f32_e32 v112, v129, v129
	v_add_f32_e32 v111, v111, v112
	v_fmac_f32_e32 v121, 0xba000000, v110
	v_fmac_f32_e32 v119, 0xba000000, v110
	v_add_f32_e32 v2, v111, v2
	v_fmac_f32_e32 v120, 0xba000000, v110
	v_fmac_f32_e32 v118, 0xba000000, v110
	v_mul_f32_e32 v111, v119, v119
	v_mul_f32_e32 v112, v121, v121
	v_fmac_f32_e32 v111, v118, v118
	v_fmac_f32_e32 v112, v120, v120
	v_add_f32_e32 v111, v111, v112
	v_fmac_f32_e32 v115, 0xba000000, v110
	v_fmac_f32_e32 v117, 0xba000000, v110
	v_add_f32_e32 v2, v111, v2
	v_fmac_f32_e32 v113, 0xba000000, v110
	v_fmac_f32_e32 v116, 0xba000000, v110
	v_mul_f32_e32 v111, v117, v117
	v_mul_f32_e32 v112, v115, v115
	v_fmac_f32_e32 v111, v116, v116
	v_fmac_f32_e32 v112, v113, v113
	v_add_f32_e32 v111, v111, v112
	v_add_f32_e32 v2, v111, v2
	s_waitcnt lgkmcnt(0)
	s_nop 1
	v_add_f32_dpp v2, v2, v2 quad_perm:[1,0,3,2] row_mask:0xf bank_mask:0xf
	s_waitcnt lgkmcnt(0)
	s_nop 1
	v_add_f32_dpp v2, v2, v2 quad_perm:[2,3,0,1] row_mask:0xf bank_mask:0xf
	s_waitcnt lgkmcnt(0)
	s_nop 1
	v_add_f32_dpp v2, v2, v2 row_half_mirror row_mask:0xf bank_mask:0xf
	s_waitcnt lgkmcnt(0)
	s_nop 1
	v_add_f32_dpp v2, v2, v2 row_mirror row_mask:0xf bank_mask:0xf
	s_waitcnt lgkmcnt(0)
	v_mov_b32_e32 v111, v2
	s_nop 1
	v_permlane16_swap_b32_e32 v111, v2
	v_add_f32_e32 v2, v2, v111
	s_waitcnt lgkmcnt(0)
	v_mov_b32_e32 v111, v2
	s_nop 1
	v_permlane32_swap_b32_e32 v111, v2
	v_add_f32_e32 v2, v2, v111
	v_fmamk_f32 v2, v2, 0x3a000000, v217
	v_cmp_gt_f32_e32 vcc, s87, v2
	v_mul_f32_e32 v111, 0x4f800000, v2
	s_nop 0
	v_cndmask_b32_e32 v2, v2, v111, vcc
	v_sqrt_f32_e32 v111, v2
	s_nop 0
	v_add_u32_e32 v112, -1, v111
	v_fma_f32 v114, -v112, v111, v2
	v_cmp_ge_f32_e64 s[8:9], 0, v114
	v_add_u32_e32 v114, 1, v111
	s_nop 0
	v_cndmask_b32_e64 v112, v111, v112, s[8:9]
	v_fma_f32 v111, -v114, v111, v2
	v_cmp_lt_f32_e64 s[8:9], 0, v111
	s_nop 1
	v_cndmask_b32_e64 v111, v112, v114, s[8:9]
	v_mul_f32_e32 v112, 0x37800000, v111
	v_cndmask_b32_e32 v111, v111, v112, vcc
	v_cmp_class_f32_e32 vcc, v2, v218
	s_nop 1
	v_cndmask_b32_e32 v2, v111, v2, vcc
	v_div_scale_f32 v111, s[8:9], v2, v2, 1.0
	v_rcp_f32_e32 v112, v111
	s_nop 0
	v_fma_f32 v114, -v111, v112, 1.0
	v_fmac_f32_e32 v112, v114, v112
	v_div_scale_f32 v114, vcc, 1.0, v2, 1.0
	v_mul_f32_e32 v122, v114, v112
	v_fma_f32 v124, -v111, v122, v114
	v_fmac_f32_e32 v122, v124, v112
	v_fma_f32 v111, -v111, v122, v114
	v_div_fmas_f32 v111, v111, v112, v122
	v_div_fixup_f32 v2, v111, v2, 1.0
	s_and_saveexec_b64 s[8:9], s[4:5]
	s_add_i32 s10, s78, 0
	v_mul_f32_e32 v110, 0x3a000000, v110
	v_mov_b32_e32 v111, v2
	v_mov_b32_e32 v112, s10
	ds_write_b64 v112, v[110:111] offset:33848
	s_or_b64 exec, exec, s[8:9]
	v_mov_b32_e32 v110, v146
	v_mov_b32_e32 v111, v136
	v_mov_b32_e32 v150, v142
	v_mov_b32_e32 v151, v144
	v_pk_mul_f32 v[150:151], v[150:151], v[2:3] op_sel_hi:[1,0]
	v_pk_mul_f32 v[110:111], v[110:111], v[2:3] op_sel_hi:[1,0]
	s_movk_i32 s8, 0x7000
	v_mov_b32_e32 v136, v147
	v_pk_fma_f32 v[104:105], v[104:105], v[150:151], v[108:109]
	v_pk_fma_f32 v[102:103], v[102:103], v[110:111], v[106:107]
	v_add_co_u32_e32 v4, vcc, s8, v4
	v_cvt_pk_bf16_f32 v102, v102, v103
	v_cvt_pk_bf16_f32 v103, v104, v105
	v_mov_b32_e32 v144, v143
	s_nop 0
	v_addc_co_u32_e32 v5, vcc, 0, v5, vcc
	v_pk_mul_f32 v[104:105], v[136:137], v[2:3] op_sel_hi:[1,0]
	global_store_dwordx2 v[4:5], v[102:103], off
	v_pk_mul_f32 v[102:103], v[144:145], v[2:3] op_sel_hi:[1,0]
	v_pk_fma_f32 v[94:95], v[94:95], v[104:105], v[98:99]
	v_mov_b32_e32 v146, v138
	v_mov_b32_e32 v147, v140
	v_pk_fma_f32 v[96:97], v[96:97], v[102:103], v[100:101]
	v_cvt_pk_bf16_f32 v94, v94, v95
	v_mov_b32_e32 v140, v139
	v_cvt_pk_bf16_f32 v95, v96, v97
	global_store_dwordx2 v[4:5], v[94:95], off offset:512
	v_pk_mul_f32 v[94:95], v[140:141], v[2:3] op_sel_hi:[1,0]
	v_pk_mul_f32 v[96:97], v[146:147], v[2:3] op_sel_hi:[1,0]
	v_pk_fma_f32 v[88:89], v[88:89], v[94:95], v[92:93]
	v_pk_fma_f32 v[86:87], v[86:87], v[96:97], v[90:91]
	v_mov_b32_e32 v126, v149
	v_cvt_pk_bf16_f32 v86, v86, v87
	v_cvt_pk_bf16_f32 v87, v88, v89
	v_pk_mul_f32 v[88:89], v[132:133], v[2:3] op_sel_hi:[1,0]
	global_store_dwordx2 v[4:5], v[86:87], off offset:1024
	v_pk_mul_f32 v[86:87], v[134:135], v[2:3] op_sel_hi:[1,0]
	v_pk_fma_f32 v[78:79], v[78:79], v[88:89], v[82:83]
	v_pk_fma_f32 v[80:81], v[80:81], v[86:87], v[84:85]
	v_cvt_pk_bf16_f32 v78, v78, v79
	v_mov_b32_e32 v124, v123
	v_cvt_pk_bf16_f32 v79, v80, v81
	global_store_dwordx2 v[4:5], v[78:79], off offset:1536
	v_pk_mul_f32 v[78:79], v[124:125], v[2:3] op_sel_hi:[1,0]
	v_pk_mul_f32 v[80:81], v[126:127], v[2:3] op_sel_hi:[1,0]
	v_mov_b32_e32 v148, v128
	v_mov_b32_e32 v149, v130
	v_pk_fma_f32 v[72:73], v[72:73], v[78:79], v[76:77]
	v_pk_fma_f32 v[70:71], v[70:71], v[80:81], v[74:75]
	v_mov_b32_e32 v130, v129
	v_cvt_pk_bf16_f32 v70, v70, v71
	v_cvt_pk_bf16_f32 v71, v72, v73
	v_pk_mul_f32 v[72:73], v[148:149], v[2:3] op_sel_hi:[1,0]
	global_store_dwordx2 v[4:5], v[70:71], off offset:2048
	v_pk_mul_f32 v[70:71], v[130:131], v[2:3] op_sel_hi:[1,0]
	v_pk_fma_f32 v[62:63], v[62:63], v[72:73], v[66:67]
	v_pk_fma_f32 v[64:65], v[64:65], v[70:71], v[68:69]
	v_cvt_pk_bf16_f32 v62, v62, v63
	v_mov_b32_e32 v114, v113
	v_cvt_pk_bf16_f32 v63, v64, v65
	global_store_dwordx2 v[4:5], v[62:63], off offset:2560
	v_pk_mul_f32 v[62:63], v[120:121], v[2:3] op_sel_hi:[1,0]
	v_pk_mul_f32 v[64:65], v[118:119], v[2:3] op_sel_hi:[1,0]
	v_pk_fma_f32 v[56:57], v[56:57], v[62:63], v[60:61]
	v_pk_fma_f32 v[54:55], v[54:55], v[64:65], v[58:59]
	s_nop 0
	v_cvt_pk_bf16_f32 v54, v54, v55
	v_cvt_pk_bf16_f32 v55, v56, v57
	v_pk_mul_f32 v[56:57], v[116:117], v[2:3] op_sel_hi:[1,0]
	global_store_dwordx2 v[4:5], v[54:55], off offset:3072
	v_pk_mul_f32 v[54:55], v[114:115], v[2:3] op_sel_hi:[1,0]
	v_pk_fma_f32 v[46:47], v[46:47], v[56:57], v[50:51]
	v_pk_fma_f32 v[48:49], v[48:49], v[54:55], v[52:53]
	v_cvt_pk_bf16_f32 v46, v46, v47
	s_nop 0
	v_cvt_pk_bf16_f32 v47, v48, v49
	global_store_dwordx2 v[4:5], v[46:47], off offset:3584
	s_waitcnt vmcnt(0) lgkmcnt(0)
	s_and_saveexec_b64 s[8:9], s[4:5]
	s_xor_b64 s[8:9], exec, s[8:9]
	s_cbranch_execz .LBB0_1459
	s_mov_b64 s[12:13], exec
	v_mbcnt_lo_u32_b32 v2, s12, 0
	v_mbcnt_hi_u32_b32 v2, s13, v2
	v_cmp_eq_u32_e32 vcc, 0, v2
	s_and_saveexec_b64 s[10:11], vcc
	s_bcnt1_i32_b64 s12, s[12:13]
	v_mov_b32_e32 v2, s88
	v_mov_b32_e32 v4, s12
	ds_add_u32 v2, v4
	s_or_b64 exec, exec, s[10:11]
